# pool/conv elementwise pass of P2 rewritten by hand (4-row blocks, window rows loaded once, all loads in flight) on top of the late-conversion changes
# speedup vs baseline: 1.0088x; 1.0033x over previous
;     __device__ __forceinline__ const char* pb(const Unit& u) const { return (const char*)(Bt + ((size_t)u.pn * BM * ldb + (size_t)u.sub * b_sub)); }
; __device__ __forceinline__ unsigned pk2(float lo, float hi) { return pg8::cvt_pk_bf16(lo, hi); }
; __device__ __forceinline__ void unpack8(const v4u w, float (&f)[8]) { f[0] = bflo(w.x); f[1] = bfhi(w.x); f[2] = bflo(w.y); f[3] = bfhi(w.y); f[4] = bflo(w.z); f[5] = bfhi(w.z); f[6] = bflo(w.w); f[7] = bfhi(w.w); }
; __device__ __forceinline__ int lane_id() { int l; asm volatile("s_nop 4\n\tv_mbcnt_lo_u32_b32 %0, -1, 0\n\tv_mbcnt_hi_u32_b32 %0, -1, %0\n\ts_nop 4" : "=v"(l)); return l; }
; template <int W> __device__ __forceinline__ void pool_item(Frame& F, int row, int t, int c8) {
;     float s[8], u[8];
; #pragma unroll
;     for (int i = 0; i < 8; ++i) s[i] = 0.f;
;     v4u ld[W];
; #pragma unroll
;     for (int k = 0; k < W; ++k) { const int kk = (t - k) >= 0 ? k : t; ld[k] = *(const v4u*)(F.PROJ + (size_t)(row - kk) * INWP + O_UPOOL + c8); }
; #pragma unroll
;     for (int k = W - 1; k >= 0; --k) { unpack8(ld[k], u); const float wgt = (t - k) >= 0 ? 1.f : 0.f;
; #pragma unroll
;         for (int i = 0; i < 8; ++i) s[i] += wgt * u[i]; }
;     const int cnt = (t + 1) < W ? (t + 1) : W;
;     const float inv = 1.0f / (float)cnt;
;     v4u o; o.x = pk2(s[0] * inv - u[0], s[1] * inv - u[1]); o.y = pk2(s[2] * inv - u[2], s[3] * inv - u[3]); o.z = pk2(s[4] * inv - u[4], s[5] * inv - u[5]); o.w = pk2(s[6] * inv - u[6], s[7] * inv - u[7]);
;     *(v4u*)(F.Y + (size_t)row * 1024 + c8) = o;
; }
; __device__ __forceinline__ void poolconv_phase(Frame& F, const float* conv_w_l) {
;     int tid = F.wave * 64 + lane_id(); asm volatile("" : "+v"(tid));
;     const int gt = F.vcu * NTHR + tid, NGT = F.G * NTHR;
;     for (int idx = gt; idx < M * 128; idx += NGT) {
;         const int grp = idx / (M * 32), rem = idx - grp * (M * 32), row = rem >> 5, c8 = grp * 256 + (rem & 31) * 8, t = row & (SEQ - 1);
;         if (grp == 0) pool_item<2>(F, row, t, c8); else if (grp == 1) pool_item<4>(F, row, t, c8); else if (grp == 2) pool_item<8>(F, row, t, c8); else pool_item<16>(F, row, t, c8);
; __global__ void __launch_bounds__(NTHR, 2) mk_fwd(Args args) {
;     ...
;         if (IN(pb + 1)) { poolconv_phase(F, F.conv_w + (size_t)l * 3 * 1024); scores_phase_mfma(F); GRID_BAR(); }
.LBB0_239:
	v_readlane_b32 s0, v255, 42
	s_add_i32 s4, s0, 2
	v_readlane_b32 s0, v251, 14
	v_readlane_b32 s1, v251, 15
	s_cmp_le_i32 s0, s4
	s_cselect_b64 s[2:3], -1, 0
	s_cmp_lt_i32 s4, s1
	s_cselect_b64 s[4:5], -1, 0
	s_mov_b32 s1, s63
	s_and_b64 s[2:3], s[2:3], s[4:5]
	v_writelane_b32 v255, s0, 45
	s_andn2_b64 vcc, exec, s[2:3]
	s_nop 0
	v_writelane_b32 v255, s1, 46
	s_cbranch_vccnz .LBB0_540
	v_mbcnt_lo_u32_b32 v0, -1, 0
	v_mbcnt_hi_u32_b32 v0, -1, v0
	v_readlane_b32 s0, v255, 12
	v_readlane_b32 s14, v251, 40
	v_readlane_b32 s15, v251, 41
	v_readlane_b32 s10, v255, 43
	s_and_b32 s1, s0, 7
	s_lshl_b32 s1, s1, 5
	s_lshr_b32 s0, s0, 3
	s_or_b32 s1, s1, s0
	s_lshl_b32 s2, s1, 9
	s_lshl_b32 s3, s35, 6
	s_add_i32 s2, s2, s3
	v_add_u32_e32 v1, s2, v0
	s_lshr_b32 s3, s1, 7
	v_and_b32_e32 v2, 0xffff, v1
	v_lshrrev_b32_e32 v2, 5, v2
	v_and_b32_e32 v3, 31, v1
	v_lshlrev_b32_e32 v4, 2, v2
	v_and_b32_e32 v5, 0x7ff, v4
	v_mul_u32_u24_e32 v6, 0x3600, v5
	v_mul_u32_u24_e32 v7, 0x3600, v4
	v_lshlrev_b32_e32 v8, 4, v3
	v_lshl_add_u32 v9, v4, 11, v8
	v_add_u32_e32 v7, v7, v8
	s_cmp_eq_u32 s3, 0
	s_cbranch_scc0 .Lpc_g1
	v_add_u32_e32 v14, 0x0, v7
	v_add_u32_e32 v15, 0x600, v7
	v_add_u32_e32 v16, 0x0, v9
	v_add_u32_e32 v17, 0x600, v9
	v_min_u32_e32 v11, 0x3600, v6
	v_sub_u32_e32 v12, v14, v11
	global_load_dwordx4 v[20:23], v12, s[96:97]
	global_load_dwordx4 v[24:27], v14, s[96:97]
	v_add_u32_e32 v12, 0x3600, v14
	global_load_dwordx4 v[28:31], v12, s[96:97]
	v_add_u32_e32 v12, 0x6c00, v14
	global_load_dwordx4 v[32:35], v12, s[96:97]
	v_add_u32_e32 v12, 0xa200, v14
	global_load_dwordx4 v[36:39], v12, s[96:97]
	v_min_u32_e32 v11, 0x32a00, v6
	v_sub_u32_e32 v12, v15, v11
	global_load_dwordx4 v[48:51], v12, s[96:97]
	v_min_u32_e32 v11, 0x2f400, v6
	v_sub_u32_e32 v12, v15, v11
	global_load_dwordx4 v[52:55], v12, s[96:97]
	v_min_u32_e32 v11, 0x2be00, v6
	v_sub_u32_e32 v12, v15, v11
	global_load_dwordx4 v[56:59], v12, s[96:97]
	v_min_u32_e32 v11, 0x28800, v6
	v_sub_u32_e32 v12, v15, v11
	global_load_dwordx4 v[60:63], v12, s[96:97]
	v_min_u32_e32 v11, 0x25200, v6
	v_sub_u32_e32 v12, v15, v11
	global_load_dwordx4 v[64:67], v12, s[96:97]
	v_min_u32_e32 v11, 0x21c00, v6
	v_sub_u32_e32 v12, v15, v11
	global_load_dwordx4 v[68:71], v12, s[96:97]
	v_min_u32_e32 v11, 0x1e600, v6
	v_sub_u32_e32 v12, v15, v11
	global_load_dwordx4 v[72:75], v12, s[96:97]
	v_min_u32_e32 v11, 0x1b000, v6
	v_sub_u32_e32 v12, v15, v11
	global_load_dwordx4 v[76:79], v12, s[96:97]
	v_min_u32_e32 v11, 0x17a00, v6
	v_sub_u32_e32 v12, v15, v11
	global_load_dwordx4 v[80:83], v12, s[96:97]
	v_min_u32_e32 v11, 0x14400, v6
	v_sub_u32_e32 v12, v15, v11
	global_load_dwordx4 v[84:87], v12, s[96:97]
	v_min_u32_e32 v11, 0x10e00, v6
	v_sub_u32_e32 v12, v15, v11
	global_load_dwordx4 v[88:91], v12, s[96:97]
	v_min_u32_e32 v11, 0xd800, v6
	v_sub_u32_e32 v12, v15, v11
	global_load_dwordx4 v[92:95], v12, s[96:97]
	v_min_u32_e32 v11, 0xa200, v6
	v_sub_u32_e32 v12, v15, v11
	global_load_dwordx4 v[96:99], v12, s[96:97]
	v_min_u32_e32 v11, 0x6c00, v6
	v_sub_u32_e32 v12, v15, v11
	global_load_dwordx4 v[100:103], v12, s[96:97]
	v_min_u32_e32 v11, 0x3600, v6
	v_sub_u32_e32 v12, v15, v11
	global_load_dwordx4 v[104:107], v12, s[96:97]
	global_load_dwordx4 v[108:111], v15, s[96:97]
	v_add_u32_e32 v12, 0x3600, v15
	global_load_dwordx4 v[112:115], v12, s[96:97]
	v_add_u32_e32 v12, 0x6c00, v15
	global_load_dwordx4 v[116:119], v12, s[96:97]
	v_add_u32_e32 v12, 0xa200, v15
	global_load_dwordx4 v[120:123], v12, s[96:97]
	s_waitcnt vmcnt(19)
	v_cmp_le_u32_e32 vcc, 1, v5
	s_nop 1
	v_cndmask_b32_e32 v20, 0, v20, vcc
	v_cndmask_b32_e32 v21, 0, v21, vcc
	v_cndmask_b32_e32 v22, 0, v22, vcc
	v_cndmask_b32_e32 v23, 0, v23, vcc
	v_add_u32_e32 v226, 1, v5
	v_min_u32_e32 v226, 2, v226
	v_cvt_f32_u32_e32 v226, v226
	v_rcp_f32_e32 v226, v226
	v_add_u32_e32 v227, 2, v5
	v_min_u32_e32 v227, 2, v227
	v_cvt_f32_u32_e32 v227, v227
	v_rcp_f32_e32 v227, v227
	v_add_u32_e32 v228, 3, v5
	v_min_u32_e32 v228, 2, v228
	v_cvt_f32_u32_e32 v228, v228
	v_rcp_f32_e32 v228, v228
	v_add_u32_e32 v229, 4, v5
	v_min_u32_e32 v229, 2, v229
	v_cvt_f32_u32_e32 v229, v229
	v_rcp_f32_e32 v229, v229
	v_lshlrev_b32_e32 v124, 16, v20
	v_and_b32_e32 v125, 0xffff0000, v20
	v_lshlrev_b32_e32 v126, 16, v24
	v_and_b32_e32 v127, 0xffff0000, v24
	v_lshlrev_b32_e32 v128, 16, v28
	v_and_b32_e32 v129, 0xffff0000, v28
	v_lshlrev_b32_e32 v130, 16, v32
	v_and_b32_e32 v131, 0xffff0000, v32
	v_lshlrev_b32_e32 v132, 16, v36
	v_and_b32_e32 v133, 0xffff0000, v36
	v_add_f32_e32 v194, v124, v126
	v_fma_f32 v194, v194, v226, -v126
	v_add_f32_e32 v195, v125, v127
	v_fma_f32 v195, v195, v226, -v127
	v_add_f32_e32 v202, v126, v128
	v_fma_f32 v202, v202, v227, -v128
	v_add_f32_e32 v203, v127, v129
	v_fma_f32 v203, v203, v227, -v129
	v_add_f32_e32 v210, v128, v130
	v_fma_f32 v210, v210, v228, -v130
	v_add_f32_e32 v211, v129, v131
	v_fma_f32 v211, v211, v228, -v131
	v_add_f32_e32 v218, v130, v132
	v_fma_f32 v218, v218, v229, -v132
	v_add_f32_e32 v219, v131, v133
	v_fma_f32 v219, v219, v229, -v133
	v_lshlrev_b32_e32 v124, 16, v21
	v_and_b32_e32 v125, 0xffff0000, v21
	v_lshlrev_b32_e32 v126, 16, v25
	v_and_b32_e32 v127, 0xffff0000, v25
	v_lshlrev_b32_e32 v128, 16, v29
	v_and_b32_e32 v129, 0xffff0000, v29
	v_lshlrev_b32_e32 v130, 16, v33
	v_and_b32_e32 v131, 0xffff0000, v33
	v_lshlrev_b32_e32 v132, 16, v37
	v_and_b32_e32 v133, 0xffff0000, v37
	v_add_f32_e32 v196, v124, v126
	v_fma_f32 v196, v196, v226, -v126
	v_add_f32_e32 v197, v125, v127
	v_fma_f32 v197, v197, v226, -v127
	v_add_f32_e32 v204, v126, v128
	v_fma_f32 v204, v204, v227, -v128
	v_add_f32_e32 v205, v127, v129
	v_fma_f32 v205, v205, v227, -v129
; __device__ __forceinline__ unsigned pk2(float lo, float hi) { return pg8::cvt_pk_bf16(lo, hi); }
; __device__ __forceinline__ void unpack8(const v4u w, float (&f)[8]) { f[0] = bflo(w.x); f[1] = bfhi(w.x); f[2] = bflo(w.y); f[3] = bfhi(w.y); f[4] = bflo(w.z); f[5] = bfhi(w.z); f[6] = bflo(w.w); f[7] = bfhi(w.w); }
; template <int W> __device__ __forceinline__ void pool_item(Frame& F, int row, int t, int c8) {
;     float s[8], u[8];
; #pragma unroll
;     for (int i = 0; i < 8; ++i) s[i] = 0.f;
;     v4u ld[W];
; #pragma unroll
;     for (int k = 0; k < W; ++k) { const int kk = (t - k) >= 0 ? k : t; ld[k] = *(const v4u*)(F.PROJ + (size_t)(row - kk) * INWP + O_UPOOL + c8); }
; #pragma unroll
;     for (int k = W - 1; k >= 0; --k) { unpack8(ld[k], u); const float wgt = (t - k) >= 0 ? 1.f : 0.f;
; #pragma unroll
;         for (int i = 0; i < 8; ++i) s[i] += wgt * u[i]; }
;     const int cnt = (t + 1) < W ? (t + 1) : W;
;     const float inv = 1.0f / (float)cnt;
;     v4u o; o.x = pk2(s[0] * inv - u[0], s[1] * inv - u[1]); o.y = pk2(s[2] * inv - u[2], s[3] * inv - u[3]); o.z = pk2(s[4] * inv - u[4], s[5] * inv - u[5]); o.w = pk2(s[6] * inv - u[6], s[7] * inv - u[7]);
;     *(v4u*)(F.Y + (size_t)row * 1024 + c8) = o;
; }
	v_add_f32_e32 v212, v128, v130
	v_fma_f32 v212, v212, v228, -v130
	v_add_f32_e32 v213, v129, v131
	v_fma_f32 v213, v213, v228, -v131
	v_add_f32_e32 v220, v130, v132
	v_fma_f32 v220, v220, v229, -v132
	v_add_f32_e32 v221, v131, v133
	v_fma_f32 v221, v221, v229, -v133
	v_lshlrev_b32_e32 v124, 16, v22
	v_and_b32_e32 v125, 0xffff0000, v22
	v_lshlrev_b32_e32 v126, 16, v26
	v_and_b32_e32 v127, 0xffff0000, v26
	v_lshlrev_b32_e32 v128, 16, v30
	v_and_b32_e32 v129, 0xffff0000, v30
	v_lshlrev_b32_e32 v130, 16, v34
	v_and_b32_e32 v131, 0xffff0000, v34
	v_lshlrev_b32_e32 v132, 16, v38
	v_and_b32_e32 v133, 0xffff0000, v38
	v_add_f32_e32 v198, v124, v126
	v_fma_f32 v198, v198, v226, -v126
	v_add_f32_e32 v199, v125, v127
	v_fma_f32 v199, v199, v226, -v127
	v_add_f32_e32 v206, v126, v128
	v_fma_f32 v206, v206, v227, -v128
	v_add_f32_e32 v207, v127, v129
	v_fma_f32 v207, v207, v227, -v129
	v_add_f32_e32 v214, v128, v130
	v_fma_f32 v214, v214, v228, -v130
	v_add_f32_e32 v215, v129, v131
	v_fma_f32 v215, v215, v228, -v131
	v_add_f32_e32 v222, v130, v132
	v_fma_f32 v222, v222, v229, -v132
	v_add_f32_e32 v223, v131, v133
	v_fma_f32 v223, v223, v229, -v133
	v_lshlrev_b32_e32 v124, 16, v23
	v_and_b32_e32 v125, 0xffff0000, v23
	v_lshlrev_b32_e32 v126, 16, v27
	v_and_b32_e32 v127, 0xffff0000, v27
	v_lshlrev_b32_e32 v128, 16, v31
	v_and_b32_e32 v129, 0xffff0000, v31
	v_lshlrev_b32_e32 v130, 16, v35
	v_and_b32_e32 v131, 0xffff0000, v35
	v_lshlrev_b32_e32 v132, 16, v39
	v_and_b32_e32 v133, 0xffff0000, v39
	v_add_f32_e32 v200, v124, v126
	v_fma_f32 v200, v200, v226, -v126
	v_add_f32_e32 v201, v125, v127
	v_fma_f32 v201, v201, v226, -v127
	v_add_f32_e32 v208, v126, v128
	v_fma_f32 v208, v208, v227, -v128
	v_add_f32_e32 v209, v127, v129
	v_fma_f32 v209, v209, v227, -v129
	v_add_f32_e32 v216, v128, v130
	v_fma_f32 v216, v216, v228, -v130
	v_add_f32_e32 v217, v129, v131
	v_fma_f32 v217, v217, v228, -v131
	v_add_f32_e32 v224, v130, v132
	v_fma_f32 v224, v224, v229, -v132
	v_add_f32_e32 v225, v131, v133
	v_fma_f32 v225, v225, v229, -v133
	v_cvt_pk_bf16_f32 v194, v194, v195
	v_cvt_pk_bf16_f32 v195, v196, v197
	v_cvt_pk_bf16_f32 v196, v198, v199
	v_cvt_pk_bf16_f32 v197, v200, v201
	global_store_dwordx4 v16, v[194:197], s[14:15]
	v_cvt_pk_bf16_f32 v202, v202, v203
	v_cvt_pk_bf16_f32 v203, v204, v205
	v_cvt_pk_bf16_f32 v204, v206, v207
	v_cvt_pk_bf16_f32 v205, v208, v209
	v_add_u32_e32 v13, 0x800, v16
	global_store_dwordx4 v13, v[202:205], s[14:15]
	v_cvt_pk_bf16_f32 v210, v210, v211
	v_cvt_pk_bf16_f32 v211, v212, v213
	v_cvt_pk_bf16_f32 v212, v214, v215
	v_cvt_pk_bf16_f32 v213, v216, v217
	v_add_u32_e32 v13, 0x1000, v16
	global_store_dwordx4 v13, v[210:213], s[14:15]
	v_cvt_pk_bf16_f32 v218, v218, v219
	v_cvt_pk_bf16_f32 v219, v220, v221
	v_cvt_pk_bf16_f32 v220, v222, v223
	v_cvt_pk_bf16_f32 v221, v224, v225
	v_add_u32_e32 v13, 0x1800, v16
	global_store_dwordx4 v13, v[218:221], s[14:15]
	s_waitcnt vmcnt(4)
	v_cmp_le_u32_e32 vcc, 15, v5
	s_nop 1
	v_cndmask_b32_e32 v48, 0, v48, vcc
	v_cndmask_b32_e32 v49, 0, v49, vcc
	v_cndmask_b32_e32 v50, 0, v50, vcc
	v_cndmask_b32_e32 v51, 0, v51, vcc
	v_cmp_le_u32_e32 vcc, 14, v5
	s_nop 1
	v_cndmask_b32_e32 v52, 0, v52, vcc
	v_cndmask_b32_e32 v53, 0, v53, vcc
	v_cndmask_b32_e32 v54, 0, v54, vcc
	v_cndmask_b32_e32 v55, 0, v55, vcc
	v_cmp_le_u32_e32 vcc, 13, v5
	s_nop 1
	v_cndmask_b32_e32 v56, 0, v56, vcc
	v_cndmask_b32_e32 v57, 0, v57, vcc
	v_cndmask_b32_e32 v58, 0, v58, vcc
	v_cndmask_b32_e32 v59, 0, v59, vcc
	v_cmp_le_u32_e32 vcc, 12, v5
	s_nop 1
	v_cndmask_b32_e32 v60, 0, v60, vcc
	v_cndmask_b32_e32 v61, 0, v61, vcc
	v_cndmask_b32_e32 v62, 0, v62, vcc
	v_cndmask_b32_e32 v63, 0, v63, vcc
	v_cmp_le_u32_e32 vcc, 11, v5
	s_nop 1
	v_cndmask_b32_e32 v64, 0, v64, vcc
	v_cndmask_b32_e32 v65, 0, v65, vcc
	v_cndmask_b32_e32 v66, 0, v66, vcc
	v_cndmask_b32_e32 v67, 0, v67, vcc
	v_cmp_le_u32_e32 vcc, 10, v5
	s_nop 1
	v_cndmask_b32_e32 v68, 0, v68, vcc
	v_cndmask_b32_e32 v69, 0, v69, vcc
	v_cndmask_b32_e32 v70, 0, v70, vcc
	v_cndmask_b32_e32 v71, 0, v71, vcc
	v_cmp_le_u32_e32 vcc, 9, v5
	s_nop 1
	v_cndmask_b32_e32 v72, 0, v72, vcc
	v_cndmask_b32_e32 v73, 0, v73, vcc
	v_cndmask_b32_e32 v74, 0, v74, vcc
	v_cndmask_b32_e32 v75, 0, v75, vcc
	v_cmp_le_u32_e32 vcc, 8, v5
	s_nop 1
	v_cndmask_b32_e32 v76, 0, v76, vcc
	v_cndmask_b32_e32 v77, 0, v77, vcc
	v_cndmask_b32_e32 v78, 0, v78, vcc
	v_cndmask_b32_e32 v79, 0, v79, vcc
	v_cmp_le_u32_e32 vcc, 7, v5
	s_nop 1
	v_cndmask_b32_e32 v80, 0, v80, vcc
	v_cndmask_b32_e32 v81, 0, v81, vcc
	v_cndmask_b32_e32 v82, 0, v82, vcc
	v_cndmask_b32_e32 v83, 0, v83, vcc
	v_cmp_le_u32_e32 vcc, 6, v5
	s_nop 1
	v_cndmask_b32_e32 v84, 0, v84, vcc
	v_cndmask_b32_e32 v85, 0, v85, vcc
	v_cndmask_b32_e32 v86, 0, v86, vcc
	v_cndmask_b32_e32 v87, 0, v87, vcc
	v_cmp_le_u32_e32 vcc, 5, v5
	s_nop 1
	v_cndmask_b32_e32 v88, 0, v88, vcc
	v_cndmask_b32_e32 v89, 0, v89, vcc
	v_cndmask_b32_e32 v90, 0, v90, vcc
	v_cndmask_b32_e32 v91, 0, v91, vcc
	v_cmp_le_u32_e32 vcc, 4, v5
	s_nop 1
	v_cndmask_b32_e32 v92, 0, v92, vcc
	v_cndmask_b32_e32 v93, 0, v93, vcc
	v_cndmask_b32_e32 v94, 0, v94, vcc
	v_cndmask_b32_e32 v95, 0, v95, vcc
	v_cmp_le_u32_e32 vcc, 3, v5
	s_nop 1
	v_cndmask_b32_e32 v96, 0, v96, vcc
	v_cndmask_b32_e32 v97, 0, v97, vcc
	v_cndmask_b32_e32 v98, 0, v98, vcc
	v_cndmask_b32_e32 v99, 0, v99, vcc
	v_cmp_le_u32_e32 vcc, 2, v5
	s_nop 1
	v_cndmask_b32_e32 v100, 0, v100, vcc
	v_cndmask_b32_e32 v101, 0, v101, vcc
	v_cndmask_b32_e32 v102, 0, v102, vcc
	v_cndmask_b32_e32 v103, 0, v103, vcc
	v_cmp_le_u32_e32 vcc, 1, v5
	s_nop 1
	v_cndmask_b32_e32 v104, 0, v104, vcc
	v_cndmask_b32_e32 v105, 0, v105, vcc
	v_cndmask_b32_e32 v106, 0, v106, vcc
; __device__ __forceinline__ unsigned pk2(float lo, float hi) { return pg8::cvt_pk_bf16(lo, hi); }
; __device__ __forceinline__ void unpack8(const v4u w, float (&f)[8]) { f[0] = bflo(w.x); f[1] = bfhi(w.x); f[2] = bflo(w.y); f[3] = bfhi(w.y); f[4] = bflo(w.z); f[5] = bfhi(w.z); f[6] = bflo(w.w); f[7] = bfhi(w.w); }
; template <int W> __device__ __forceinline__ void pool_item(Frame& F, int row, int t, int c8) {
;     float s[8], u[8];
; #pragma unroll
;     for (int i = 0; i < 8; ++i) s[i] = 0.f;
;     v4u ld[W];
; #pragma unroll
;     for (int k = 0; k < W; ++k) { const int kk = (t - k) >= 0 ? k : t; ld[k] = *(const v4u*)(F.PROJ + (size_t)(row - kk) * INWP + O_UPOOL + c8); }
; #pragma unroll
;     for (int k = W - 1; k >= 0; --k) { unpack8(ld[k], u); const float wgt = (t - k) >= 0 ? 1.f : 0.f;
; #pragma unroll
;         for (int i = 0; i < 8; ++i) s[i] += wgt * u[i]; }
;     const int cnt = (t + 1) < W ? (t + 1) : W;
;     const float inv = 1.0f / (float)cnt;
;     v4u o; o.x = pk2(s[0] * inv - u[0], s[1] * inv - u[1]); o.y = pk2(s[2] * inv - u[2], s[3] * inv - u[3]); o.z = pk2(s[4] * inv - u[4], s[5] * inv - u[5]); o.w = pk2(s[6] * inv - u[6], s[7] * inv - u[7]);
;     *(v4u*)(F.Y + (size_t)row * 1024 + c8) = o;
; }
	v_cndmask_b32_e32 v107, 0, v107, vcc
	v_add_u32_e32 v226, 1, v5
	v_min_u32_e32 v226, 16, v226
	v_cvt_f32_u32_e32 v226, v226
	v_rcp_f32_e32 v226, v226
	v_add_u32_e32 v227, 2, v5
	v_min_u32_e32 v227, 16, v227
	v_cvt_f32_u32_e32 v227, v227
	v_rcp_f32_e32 v227, v227
	v_add_u32_e32 v228, 3, v5
	v_min_u32_e32 v228, 16, v228
	v_cvt_f32_u32_e32 v228, v228
	v_rcp_f32_e32 v228, v228
	v_add_u32_e32 v229, 4, v5
	v_min_u32_e32 v229, 16, v229
	v_cvt_f32_u32_e32 v229, v229
	v_rcp_f32_e32 v229, v229
	v_lshlrev_b32_e32 v124, 16, v48
	v_and_b32_e32 v125, 0xffff0000, v48
	v_lshlrev_b32_e32 v126, 16, v52
	v_and_b32_e32 v127, 0xffff0000, v52
	v_lshlrev_b32_e32 v128, 16, v56
	v_and_b32_e32 v129, 0xffff0000, v56
	v_lshlrev_b32_e32 v130, 16, v60
	v_and_b32_e32 v131, 0xffff0000, v60
	v_lshlrev_b32_e32 v132, 16, v64
	v_and_b32_e32 v133, 0xffff0000, v64
	v_lshlrev_b32_e32 v134, 16, v68
	v_and_b32_e32 v135, 0xffff0000, v68
	v_lshlrev_b32_e32 v136, 16, v72
	v_and_b32_e32 v137, 0xffff0000, v72
	v_lshlrev_b32_e32 v138, 16, v76
	v_and_b32_e32 v139, 0xffff0000, v76
	v_lshlrev_b32_e32 v140, 16, v80
	v_and_b32_e32 v141, 0xffff0000, v80
	v_lshlrev_b32_e32 v142, 16, v84
	v_and_b32_e32 v143, 0xffff0000, v84
	v_lshlrev_b32_e32 v144, 16, v88
	v_and_b32_e32 v145, 0xffff0000, v88
	v_lshlrev_b32_e32 v146, 16, v92
	v_and_b32_e32 v147, 0xffff0000, v92
	v_lshlrev_b32_e32 v148, 16, v96
	v_and_b32_e32 v149, 0xffff0000, v96
	v_lshlrev_b32_e32 v150, 16, v100
	v_and_b32_e32 v151, 0xffff0000, v100
	v_lshlrev_b32_e32 v152, 16, v104
	v_and_b32_e32 v153, 0xffff0000, v104
	v_lshlrev_b32_e32 v154, 16, v108
	v_and_b32_e32 v155, 0xffff0000, v108
	v_lshlrev_b32_e32 v156, 16, v112
	v_and_b32_e32 v157, 0xffff0000, v112
	v_lshlrev_b32_e32 v158, 16, v116
	v_and_b32_e32 v159, 0xffff0000, v116
	v_lshlrev_b32_e32 v160, 16, v120
	v_and_b32_e32 v161, 0xffff0000, v120
	v_add_f32_e32 v194, v124, v126
	v_add_f32_e32 v194, v194, v128
	v_add_f32_e32 v194, v194, v130
	v_add_f32_e32 v194, v194, v132
	v_add_f32_e32 v194, v194, v134
	v_add_f32_e32 v194, v194, v136
	v_add_f32_e32 v194, v194, v138
	v_add_f32_e32 v194, v194, v140
	v_add_f32_e32 v194, v194, v142
	v_add_f32_e32 v194, v194, v144
	v_add_f32_e32 v194, v194, v146
	v_add_f32_e32 v194, v194, v148
	v_add_f32_e32 v194, v194, v150
	v_add_f32_e32 v194, v194, v152
	v_add_f32_e32 v194, v194, v154
	v_fma_f32 v194, v194, v226, -v154
	v_add_f32_e32 v195, v125, v127
	v_add_f32_e32 v195, v195, v129
	v_add_f32_e32 v195, v195, v131
	v_add_f32_e32 v195, v195, v133
	v_add_f32_e32 v195, v195, v135
	v_add_f32_e32 v195, v195, v137
	v_add_f32_e32 v195, v195, v139
	v_add_f32_e32 v195, v195, v141
	v_add_f32_e32 v195, v195, v143
	v_add_f32_e32 v195, v195, v145
	v_add_f32_e32 v195, v195, v147
	v_add_f32_e32 v195, v195, v149
	v_add_f32_e32 v195, v195, v151
	v_add_f32_e32 v195, v195, v153
	v_add_f32_e32 v195, v195, v155
	v_fma_f32 v195, v195, v226, -v155
	v_add_f32_e32 v202, v126, v128
	v_add_f32_e32 v202, v202, v130
	v_add_f32_e32 v202, v202, v132
	v_add_f32_e32 v202, v202, v134
	v_add_f32_e32 v202, v202, v136
	v_add_f32_e32 v202, v202, v138
	v_add_f32_e32 v202, v202, v140
	v_add_f32_e32 v202, v202, v142
	v_add_f32_e32 v202, v202, v144
	v_add_f32_e32 v202, v202, v146
	v_add_f32_e32 v202, v202, v148
	v_add_f32_e32 v202, v202, v150
	v_add_f32_e32 v202, v202, v152
	v_add_f32_e32 v202, v202, v154
	v_add_f32_e32 v202, v202, v156
	v_fma_f32 v202, v202, v227, -v156
	v_add_f32_e32 v203, v127, v129
	v_add_f32_e32 v203, v203, v131
	v_add_f32_e32 v203, v203, v133
	v_add_f32_e32 v203, v203, v135
	v_add_f32_e32 v203, v203, v137
	v_add_f32_e32 v203, v203, v139
	v_add_f32_e32 v203, v203, v141
	v_add_f32_e32 v203, v203, v143
	v_add_f32_e32 v203, v203, v145
	v_add_f32_e32 v203, v203, v147
	v_add_f32_e32 v203, v203, v149
	v_add_f32_e32 v203, v203, v151
	v_add_f32_e32 v203, v203, v153
	v_add_f32_e32 v203, v203, v155
	v_add_f32_e32 v203, v203, v157
	v_fma_f32 v203, v203, v227, -v157
	v_add_f32_e32 v210, v128, v130
	v_add_f32_e32 v210, v210, v132
	v_add_f32_e32 v210, v210, v134
	v_add_f32_e32 v210, v210, v136
	v_add_f32_e32 v210, v210, v138
	v_add_f32_e32 v210, v210, v140
	v_add_f32_e32 v210, v210, v142
	v_add_f32_e32 v210, v210, v144
	v_add_f32_e32 v210, v210, v146
	v_add_f32_e32 v210, v210, v148
	v_add_f32_e32 v210, v210, v150
	v_add_f32_e32 v210, v210, v152
	v_add_f32_e32 v210, v210, v154
	v_add_f32_e32 v210, v210, v156
	v_add_f32_e32 v210, v210, v158
	v_fma_f32 v210, v210, v228, -v158
	v_add_f32_e32 v211, v129, v131
	v_add_f32_e32 v211, v211, v133
	v_add_f32_e32 v211, v211, v135
	v_add_f32_e32 v211, v211, v137
	v_add_f32_e32 v211, v211, v139
	v_add_f32_e32 v211, v211, v141
	v_add_f32_e32 v211, v211, v143
	v_add_f32_e32 v211, v211, v145
	v_add_f32_e32 v211, v211, v147
	v_add_f32_e32 v211, v211, v149
	v_add_f32_e32 v211, v211, v151
	v_add_f32_e32 v211, v211, v153
	v_add_f32_e32 v211, v211, v155
	v_add_f32_e32 v211, v211, v157
	v_add_f32_e32 v211, v211, v159
	v_fma_f32 v211, v211, v228, -v159
	v_add_f32_e32 v218, v130, v132
	v_add_f32_e32 v218, v218, v134
	v_add_f32_e32 v218, v218, v136
	v_add_f32_e32 v218, v218, v138
	v_add_f32_e32 v218, v218, v140
	v_add_f32_e32 v218, v218, v142
	v_add_f32_e32 v218, v218, v144
	v_add_f32_e32 v218, v218, v146
	v_add_f32_e32 v218, v218, v148
	v_add_f32_e32 v218, v218, v150
	v_add_f32_e32 v218, v218, v152
	v_add_f32_e32 v218, v218, v154
	v_add_f32_e32 v218, v218, v156
	v_add_f32_e32 v218, v218, v158
	v_add_f32_e32 v218, v218, v160
	v_fma_f32 v218, v218, v229, -v160
	v_add_f32_e32 v219, v131, v133
	v_add_f32_e32 v219, v219, v135
	v_add_f32_e32 v219, v219, v137
	v_add_f32_e32 v219, v219, v139
	v_add_f32_e32 v219, v219, v141
	v_add_f32_e32 v219, v219, v143
; __device__ __forceinline__ unsigned pk2(float lo, float hi) { return pg8::cvt_pk_bf16(lo, hi); }
; __device__ __forceinline__ void unpack8(const v4u w, float (&f)[8]) { f[0] = bflo(w.x); f[1] = bfhi(w.x); f[2] = bflo(w.y); f[3] = bfhi(w.y); f[4] = bflo(w.z); f[5] = bfhi(w.z); f[6] = bflo(w.w); f[7] = bfhi(w.w); }
; template <int W> __device__ __forceinline__ void pool_item(Frame& F, int row, int t, int c8) {
;     float s[8], u[8];
; #pragma unroll
;     for (int i = 0; i < 8; ++i) s[i] = 0.f;
;     v4u ld[W];
; #pragma unroll
;     for (int k = 0; k < W; ++k) { const int kk = (t - k) >= 0 ? k : t; ld[k] = *(const v4u*)(F.PROJ + (size_t)(row - kk) * INWP + O_UPOOL + c8); }
; #pragma unroll
;     for (int k = W - 1; k >= 0; --k) { unpack8(ld[k], u); const float wgt = (t - k) >= 0 ? 1.f : 0.f;
; #pragma unroll
;         for (int i = 0; i < 8; ++i) s[i] += wgt * u[i]; }
;     const int cnt = (t + 1) < W ? (t + 1) : W;
;     const float inv = 1.0f / (float)cnt;
;     v4u o; o.x = pk2(s[0] * inv - u[0], s[1] * inv - u[1]); o.y = pk2(s[2] * inv - u[2], s[3] * inv - u[3]); o.z = pk2(s[4] * inv - u[4], s[5] * inv - u[5]); o.w = pk2(s[6] * inv - u[6], s[7] * inv - u[7]);
;     *(v4u*)(F.Y + (size_t)row * 1024 + c8) = o;
; }
	v_add_f32_e32 v219, v219, v145
	v_add_f32_e32 v219, v219, v147
	v_add_f32_e32 v219, v219, v149
	v_add_f32_e32 v219, v219, v151
	v_add_f32_e32 v219, v219, v153
	v_add_f32_e32 v219, v219, v155
	v_add_f32_e32 v219, v219, v157
	v_add_f32_e32 v219, v219, v159
	v_add_f32_e32 v219, v219, v161
	v_fma_f32 v219, v219, v229, -v161
	v_lshlrev_b32_e32 v124, 16, v49
	v_and_b32_e32 v125, 0xffff0000, v49
	v_lshlrev_b32_e32 v126, 16, v53
	v_and_b32_e32 v127, 0xffff0000, v53
	v_lshlrev_b32_e32 v128, 16, v57
	v_and_b32_e32 v129, 0xffff0000, v57
	v_lshlrev_b32_e32 v130, 16, v61
	v_and_b32_e32 v131, 0xffff0000, v61
	v_lshlrev_b32_e32 v132, 16, v65
	v_and_b32_e32 v133, 0xffff0000, v65
	v_lshlrev_b32_e32 v134, 16, v69
	v_and_b32_e32 v135, 0xffff0000, v69
	v_lshlrev_b32_e32 v136, 16, v73
	v_and_b32_e32 v137, 0xffff0000, v73
	v_lshlrev_b32_e32 v138, 16, v77
	v_and_b32_e32 v139, 0xffff0000, v77
	v_lshlrev_b32_e32 v140, 16, v81
	v_and_b32_e32 v141, 0xffff0000, v81
	v_lshlrev_b32_e32 v142, 16, v85
	v_and_b32_e32 v143, 0xffff0000, v85
	v_lshlrev_b32_e32 v144, 16, v89
	v_and_b32_e32 v145, 0xffff0000, v89
	v_lshlrev_b32_e32 v146, 16, v93
	v_and_b32_e32 v147, 0xffff0000, v93
	v_lshlrev_b32_e32 v148, 16, v97
	v_and_b32_e32 v149, 0xffff0000, v97
	v_lshlrev_b32_e32 v150, 16, v101
	v_and_b32_e32 v151, 0xffff0000, v101
	v_lshlrev_b32_e32 v152, 16, v105
	v_and_b32_e32 v153, 0xffff0000, v105
	v_lshlrev_b32_e32 v154, 16, v109
	v_and_b32_e32 v155, 0xffff0000, v109
	v_lshlrev_b32_e32 v156, 16, v113
	v_and_b32_e32 v157, 0xffff0000, v113
	v_lshlrev_b32_e32 v158, 16, v117
	v_and_b32_e32 v159, 0xffff0000, v117
	v_lshlrev_b32_e32 v160, 16, v121
	v_and_b32_e32 v161, 0xffff0000, v121
	v_add_f32_e32 v196, v124, v126
	v_add_f32_e32 v196, v196, v128
	v_add_f32_e32 v196, v196, v130
	v_add_f32_e32 v196, v196, v132
	v_add_f32_e32 v196, v196, v134
	v_add_f32_e32 v196, v196, v136
	v_add_f32_e32 v196, v196, v138
	v_add_f32_e32 v196, v196, v140
	v_add_f32_e32 v196, v196, v142
	v_add_f32_e32 v196, v196, v144
	v_add_f32_e32 v196, v196, v146
	v_add_f32_e32 v196, v196, v148
	v_add_f32_e32 v196, v196, v150
	v_add_f32_e32 v196, v196, v152
	v_add_f32_e32 v196, v196, v154
	v_fma_f32 v196, v196, v226, -v154
	v_add_f32_e32 v197, v125, v127
	v_add_f32_e32 v197, v197, v129
	v_add_f32_e32 v197, v197, v131
	v_add_f32_e32 v197, v197, v133
	v_add_f32_e32 v197, v197, v135
	v_add_f32_e32 v197, v197, v137
	v_add_f32_e32 v197, v197, v139
	v_add_f32_e32 v197, v197, v141
	v_add_f32_e32 v197, v197, v143
	v_add_f32_e32 v197, v197, v145
	v_add_f32_e32 v197, v197, v147
	v_add_f32_e32 v197, v197, v149
	v_add_f32_e32 v197, v197, v151
	v_add_f32_e32 v197, v197, v153
	v_add_f32_e32 v197, v197, v155
	v_fma_f32 v197, v197, v226, -v155
	v_add_f32_e32 v204, v126, v128
	v_add_f32_e32 v204, v204, v130
	v_add_f32_e32 v204, v204, v132
	v_add_f32_e32 v204, v204, v134
	v_add_f32_e32 v204, v204, v136
	v_add_f32_e32 v204, v204, v138
	v_add_f32_e32 v204, v204, v140
	v_add_f32_e32 v204, v204, v142
	v_add_f32_e32 v204, v204, v144
	v_add_f32_e32 v204, v204, v146
	v_add_f32_e32 v204, v204, v148
	v_add_f32_e32 v204, v204, v150
	v_add_f32_e32 v204, v204, v152
	v_add_f32_e32 v204, v204, v154
	v_add_f32_e32 v204, v204, v156
	v_fma_f32 v204, v204, v227, -v156
	v_add_f32_e32 v205, v127, v129
	v_add_f32_e32 v205, v205, v131
	v_add_f32_e32 v205, v205, v133
	v_add_f32_e32 v205, v205, v135
	v_add_f32_e32 v205, v205, v137
	v_add_f32_e32 v205, v205, v139
	v_add_f32_e32 v205, v205, v141
	v_add_f32_e32 v205, v205, v143
	v_add_f32_e32 v205, v205, v145
	v_add_f32_e32 v205, v205, v147
	v_add_f32_e32 v205, v205, v149
	v_add_f32_e32 v205, v205, v151
	v_add_f32_e32 v205, v205, v153
	v_add_f32_e32 v205, v205, v155
	v_add_f32_e32 v205, v205, v157
	v_fma_f32 v205, v205, v227, -v157
	v_add_f32_e32 v212, v128, v130
	v_add_f32_e32 v212, v212, v132
	v_add_f32_e32 v212, v212, v134
	v_add_f32_e32 v212, v212, v136
	v_add_f32_e32 v212, v212, v138
	v_add_f32_e32 v212, v212, v140
	v_add_f32_e32 v212, v212, v142
	v_add_f32_e32 v212, v212, v144
	v_add_f32_e32 v212, v212, v146
	v_add_f32_e32 v212, v212, v148
	v_add_f32_e32 v212, v212, v150
	v_add_f32_e32 v212, v212, v152
	v_add_f32_e32 v212, v212, v154
	v_add_f32_e32 v212, v212, v156
	v_add_f32_e32 v212, v212, v158
	v_fma_f32 v212, v212, v228, -v158
	v_add_f32_e32 v213, v129, v131
	v_add_f32_e32 v213, v213, v133
	v_add_f32_e32 v213, v213, v135
	v_add_f32_e32 v213, v213, v137
	v_add_f32_e32 v213, v213, v139
	v_add_f32_e32 v213, v213, v141
	v_add_f32_e32 v213, v213, v143
	v_add_f32_e32 v213, v213, v145
	v_add_f32_e32 v213, v213, v147
	v_add_f32_e32 v213, v213, v149
	v_add_f32_e32 v213, v213, v151
	v_add_f32_e32 v213, v213, v153
	v_add_f32_e32 v213, v213, v155
	v_add_f32_e32 v213, v213, v157
	v_add_f32_e32 v213, v213, v159
	v_fma_f32 v213, v213, v228, -v159
	v_add_f32_e32 v220, v130, v132
	v_add_f32_e32 v220, v220, v134
	v_add_f32_e32 v220, v220, v136
	v_add_f32_e32 v220, v220, v138
	v_add_f32_e32 v220, v220, v140
	v_add_f32_e32 v220, v220, v142
	v_add_f32_e32 v220, v220, v144
	v_add_f32_e32 v220, v220, v146
	v_add_f32_e32 v220, v220, v148
	v_add_f32_e32 v220, v220, v150
	v_add_f32_e32 v220, v220, v152
	v_add_f32_e32 v220, v220, v154
	v_add_f32_e32 v220, v220, v156
	v_add_f32_e32 v220, v220, v158
	v_add_f32_e32 v220, v220, v160
	v_fma_f32 v220, v220, v229, -v160
	v_add_f32_e32 v221, v131, v133
	v_add_f32_e32 v221, v221, v135
	v_add_f32_e32 v221, v221, v137
	v_add_f32_e32 v221, v221, v139
	v_add_f32_e32 v221, v221, v141
	v_add_f32_e32 v221, v221, v143
	v_add_f32_e32 v221, v221, v145
	v_add_f32_e32 v221, v221, v147
	v_add_f32_e32 v221, v221, v149
	v_add_f32_e32 v221, v221, v151
	v_add_f32_e32 v221, v221, v153
	v_add_f32_e32 v221, v221, v155
; __device__ __forceinline__ unsigned pk2(float lo, float hi) { return pg8::cvt_pk_bf16(lo, hi); }
; __device__ __forceinline__ void unpack8(const v4u w, float (&f)[8]) { f[0] = bflo(w.x); f[1] = bfhi(w.x); f[2] = bflo(w.y); f[3] = bfhi(w.y); f[4] = bflo(w.z); f[5] = bfhi(w.z); f[6] = bflo(w.w); f[7] = bfhi(w.w); }
; template <int W> __device__ __forceinline__ void pool_item(Frame& F, int row, int t, int c8) {
;     float s[8], u[8];
; #pragma unroll
;     for (int i = 0; i < 8; ++i) s[i] = 0.f;
;     v4u ld[W];
; #pragma unroll
;     for (int k = 0; k < W; ++k) { const int kk = (t - k) >= 0 ? k : t; ld[k] = *(const v4u*)(F.PROJ + (size_t)(row - kk) * INWP + O_UPOOL + c8); }
; #pragma unroll
;     for (int k = W - 1; k >= 0; --k) { unpack8(ld[k], u); const float wgt = (t - k) >= 0 ? 1.f : 0.f;
; #pragma unroll
;         for (int i = 0; i < 8; ++i) s[i] += wgt * u[i]; }
;     const int cnt = (t + 1) < W ? (t + 1) : W;
;     const float inv = 1.0f / (float)cnt;
;     v4u o; o.x = pk2(s[0] * inv - u[0], s[1] * inv - u[1]); o.y = pk2(s[2] * inv - u[2], s[3] * inv - u[3]); o.z = pk2(s[4] * inv - u[4], s[5] * inv - u[5]); o.w = pk2(s[6] * inv - u[6], s[7] * inv - u[7]);
;     *(v4u*)(F.Y + (size_t)row * 1024 + c8) = o;
; }
	v_add_f32_e32 v221, v221, v157
	v_add_f32_e32 v221, v221, v159
	v_add_f32_e32 v221, v221, v161
	v_fma_f32 v221, v221, v229, -v161
	v_lshlrev_b32_e32 v124, 16, v50
	v_and_b32_e32 v125, 0xffff0000, v50
	v_lshlrev_b32_e32 v126, 16, v54
	v_and_b32_e32 v127, 0xffff0000, v54
	v_lshlrev_b32_e32 v128, 16, v58
	v_and_b32_e32 v129, 0xffff0000, v58
	v_lshlrev_b32_e32 v130, 16, v62
	v_and_b32_e32 v131, 0xffff0000, v62
	v_lshlrev_b32_e32 v132, 16, v66
	v_and_b32_e32 v133, 0xffff0000, v66
	v_lshlrev_b32_e32 v134, 16, v70
	v_and_b32_e32 v135, 0xffff0000, v70
	v_lshlrev_b32_e32 v136, 16, v74
	v_and_b32_e32 v137, 0xffff0000, v74
	v_lshlrev_b32_e32 v138, 16, v78
	v_and_b32_e32 v139, 0xffff0000, v78
	v_lshlrev_b32_e32 v140, 16, v82
	v_and_b32_e32 v141, 0xffff0000, v82
	v_lshlrev_b32_e32 v142, 16, v86
	v_and_b32_e32 v143, 0xffff0000, v86
	v_lshlrev_b32_e32 v144, 16, v90
	v_and_b32_e32 v145, 0xffff0000, v90
	v_lshlrev_b32_e32 v146, 16, v94
	v_and_b32_e32 v147, 0xffff0000, v94
	v_lshlrev_b32_e32 v148, 16, v98
	v_and_b32_e32 v149, 0xffff0000, v98
	v_lshlrev_b32_e32 v150, 16, v102
	v_and_b32_e32 v151, 0xffff0000, v102
	v_lshlrev_b32_e32 v152, 16, v106
	v_and_b32_e32 v153, 0xffff0000, v106
	v_lshlrev_b32_e32 v154, 16, v110
	v_and_b32_e32 v155, 0xffff0000, v110
	v_lshlrev_b32_e32 v156, 16, v114
	v_and_b32_e32 v157, 0xffff0000, v114
	v_lshlrev_b32_e32 v158, 16, v118
	v_and_b32_e32 v159, 0xffff0000, v118
	v_lshlrev_b32_e32 v160, 16, v122
	v_and_b32_e32 v161, 0xffff0000, v122
	v_add_f32_e32 v198, v124, v126
	v_add_f32_e32 v198, v198, v128
	v_add_f32_e32 v198, v198, v130
	v_add_f32_e32 v198, v198, v132
	v_add_f32_e32 v198, v198, v134
	v_add_f32_e32 v198, v198, v136
	v_add_f32_e32 v198, v198, v138
	v_add_f32_e32 v198, v198, v140
	v_add_f32_e32 v198, v198, v142
	v_add_f32_e32 v198, v198, v144
	v_add_f32_e32 v198, v198, v146
	v_add_f32_e32 v198, v198, v148
	v_add_f32_e32 v198, v198, v150
	v_add_f32_e32 v198, v198, v152
	v_add_f32_e32 v198, v198, v154
	v_fma_f32 v198, v198, v226, -v154
	v_add_f32_e32 v199, v125, v127
	v_add_f32_e32 v199, v199, v129
	v_add_f32_e32 v199, v199, v131
	v_add_f32_e32 v199, v199, v133
	v_add_f32_e32 v199, v199, v135
	v_add_f32_e32 v199, v199, v137
	v_add_f32_e32 v199, v199, v139
	v_add_f32_e32 v199, v199, v141
	v_add_f32_e32 v199, v199, v143
	v_add_f32_e32 v199, v199, v145
	v_add_f32_e32 v199, v199, v147
	v_add_f32_e32 v199, v199, v149
	v_add_f32_e32 v199, v199, v151
	v_add_f32_e32 v199, v199, v153
	v_add_f32_e32 v199, v199, v155
	v_fma_f32 v199, v199, v226, -v155
	v_add_f32_e32 v206, v126, v128
	v_add_f32_e32 v206, v206, v130
	v_add_f32_e32 v206, v206, v132
	v_add_f32_e32 v206, v206, v134
	v_add_f32_e32 v206, v206, v136
	v_add_f32_e32 v206, v206, v138
	v_add_f32_e32 v206, v206, v140
	v_add_f32_e32 v206, v206, v142
	v_add_f32_e32 v206, v206, v144
	v_add_f32_e32 v206, v206, v146
	v_add_f32_e32 v206, v206, v148
	v_add_f32_e32 v206, v206, v150
	v_add_f32_e32 v206, v206, v152
	v_add_f32_e32 v206, v206, v154
	v_add_f32_e32 v206, v206, v156
	v_fma_f32 v206, v206, v227, -v156
	v_add_f32_e32 v207, v127, v129
	v_add_f32_e32 v207, v207, v131
	v_add_f32_e32 v207, v207, v133
	v_add_f32_e32 v207, v207, v135
	v_add_f32_e32 v207, v207, v137
	v_add_f32_e32 v207, v207, v139
	v_add_f32_e32 v207, v207, v141
	v_add_f32_e32 v207, v207, v143
	v_add_f32_e32 v207, v207, v145
	v_add_f32_e32 v207, v207, v147
	v_add_f32_e32 v207, v207, v149
	v_add_f32_e32 v207, v207, v151
	v_add_f32_e32 v207, v207, v153
	v_add_f32_e32 v207, v207, v155
	v_add_f32_e32 v207, v207, v157
	v_fma_f32 v207, v207, v227, -v157
	v_add_f32_e32 v214, v128, v130
	v_add_f32_e32 v214, v214, v132
	v_add_f32_e32 v214, v214, v134
	v_add_f32_e32 v214, v214, v136
	v_add_f32_e32 v214, v214, v138
	v_add_f32_e32 v214, v214, v140
	v_add_f32_e32 v214, v214, v142
	v_add_f32_e32 v214, v214, v144
	v_add_f32_e32 v214, v214, v146
	v_add_f32_e32 v214, v214, v148
	v_add_f32_e32 v214, v214, v150
	v_add_f32_e32 v214, v214, v152
	v_add_f32_e32 v214, v214, v154
	v_add_f32_e32 v214, v214, v156
	v_add_f32_e32 v214, v214, v158
	v_fma_f32 v214, v214, v228, -v158
	v_add_f32_e32 v215, v129, v131
	v_add_f32_e32 v215, v215, v133
	v_add_f32_e32 v215, v215, v135
	v_add_f32_e32 v215, v215, v137
	v_add_f32_e32 v215, v215, v139
	v_add_f32_e32 v215, v215, v141
	v_add_f32_e32 v215, v215, v143
	v_add_f32_e32 v215, v215, v145
	v_add_f32_e32 v215, v215, v147
	v_add_f32_e32 v215, v215, v149
	v_add_f32_e32 v215, v215, v151
	v_add_f32_e32 v215, v215, v153
	v_add_f32_e32 v215, v215, v155
	v_add_f32_e32 v215, v215, v157
	v_add_f32_e32 v215, v215, v159
	v_fma_f32 v215, v215, v228, -v159
	v_add_f32_e32 v222, v130, v132
	v_add_f32_e32 v222, v222, v134
	v_add_f32_e32 v222, v222, v136
	v_add_f32_e32 v222, v222, v138
	v_add_f32_e32 v222, v222, v140
	v_add_f32_e32 v222, v222, v142
	v_add_f32_e32 v222, v222, v144
	v_add_f32_e32 v222, v222, v146
	v_add_f32_e32 v222, v222, v148
	v_add_f32_e32 v222, v222, v150
	v_add_f32_e32 v222, v222, v152
	v_add_f32_e32 v222, v222, v154
	v_add_f32_e32 v222, v222, v156
	v_add_f32_e32 v222, v222, v158
	v_add_f32_e32 v222, v222, v160
	v_fma_f32 v222, v222, v229, -v160
	v_add_f32_e32 v223, v131, v133
	v_add_f32_e32 v223, v223, v135
	v_add_f32_e32 v223, v223, v137
	v_add_f32_e32 v223, v223, v139
	v_add_f32_e32 v223, v223, v141
	v_add_f32_e32 v223, v223, v143
	v_add_f32_e32 v223, v223, v145
	v_add_f32_e32 v223, v223, v147
	v_add_f32_e32 v223, v223, v149
	v_add_f32_e32 v223, v223, v151
	v_add_f32_e32 v223, v223, v153
	v_add_f32_e32 v223, v223, v155
	v_add_f32_e32 v223, v223, v157
	v_add_f32_e32 v223, v223, v159
	v_add_f32_e32 v223, v223, v161
	v_fma_f32 v223, v223, v229, -v161
	v_lshlrev_b32_e32 v124, 16, v51
; __device__ __forceinline__ unsigned pk2(float lo, float hi) { return pg8::cvt_pk_bf16(lo, hi); }
; __device__ __forceinline__ void unpack8(const v4u w, float (&f)[8]) { f[0] = bflo(w.x); f[1] = bfhi(w.x); f[2] = bflo(w.y); f[3] = bfhi(w.y); f[4] = bflo(w.z); f[5] = bfhi(w.z); f[6] = bflo(w.w); f[7] = bfhi(w.w); }
; template <int W> __device__ __forceinline__ void pool_item(Frame& F, int row, int t, int c8) {
;     float s[8], u[8];
; #pragma unroll
;     for (int i = 0; i < 8; ++i) s[i] = 0.f;
;     v4u ld[W];
; #pragma unroll
;     for (int k = 0; k < W; ++k) { const int kk = (t - k) >= 0 ? k : t; ld[k] = *(const v4u*)(F.PROJ + (size_t)(row - kk) * INWP + O_UPOOL + c8); }
; #pragma unroll
;     for (int k = W - 1; k >= 0; --k) { unpack8(ld[k], u); const float wgt = (t - k) >= 0 ? 1.f : 0.f;
; #pragma unroll
;         for (int i = 0; i < 8; ++i) s[i] += wgt * u[i]; }
;     const int cnt = (t + 1) < W ? (t + 1) : W;
;     const float inv = 1.0f / (float)cnt;
;     v4u o; o.x = pk2(s[0] * inv - u[0], s[1] * inv - u[1]); o.y = pk2(s[2] * inv - u[2], s[3] * inv - u[3]); o.z = pk2(s[4] * inv - u[4], s[5] * inv - u[5]); o.w = pk2(s[6] * inv - u[6], s[7] * inv - u[7]);
;     *(v4u*)(F.Y + (size_t)row * 1024 + c8) = o;
; }
	v_and_b32_e32 v125, 0xffff0000, v51
	v_lshlrev_b32_e32 v126, 16, v55
	v_and_b32_e32 v127, 0xffff0000, v55
	v_lshlrev_b32_e32 v128, 16, v59
	v_and_b32_e32 v129, 0xffff0000, v59
	v_lshlrev_b32_e32 v130, 16, v63
	v_and_b32_e32 v131, 0xffff0000, v63
	v_lshlrev_b32_e32 v132, 16, v67
	v_and_b32_e32 v133, 0xffff0000, v67
	v_lshlrev_b32_e32 v134, 16, v71
	v_and_b32_e32 v135, 0xffff0000, v71
	v_lshlrev_b32_e32 v136, 16, v75
	v_and_b32_e32 v137, 0xffff0000, v75
	v_lshlrev_b32_e32 v138, 16, v79
	v_and_b32_e32 v139, 0xffff0000, v79
	v_lshlrev_b32_e32 v140, 16, v83
	v_and_b32_e32 v141, 0xffff0000, v83
	v_lshlrev_b32_e32 v142, 16, v87
	v_and_b32_e32 v143, 0xffff0000, v87
	v_lshlrev_b32_e32 v144, 16, v91
	v_and_b32_e32 v145, 0xffff0000, v91
	v_lshlrev_b32_e32 v146, 16, v95
	v_and_b32_e32 v147, 0xffff0000, v95
	v_lshlrev_b32_e32 v148, 16, v99
	v_and_b32_e32 v149, 0xffff0000, v99
	v_lshlrev_b32_e32 v150, 16, v103
	v_and_b32_e32 v151, 0xffff0000, v103
	v_lshlrev_b32_e32 v152, 16, v107
	v_and_b32_e32 v153, 0xffff0000, v107
	v_lshlrev_b32_e32 v154, 16, v111
	v_and_b32_e32 v155, 0xffff0000, v111
	v_lshlrev_b32_e32 v156, 16, v115
	v_and_b32_e32 v157, 0xffff0000, v115
	v_lshlrev_b32_e32 v158, 16, v119
	v_and_b32_e32 v159, 0xffff0000, v119
	v_lshlrev_b32_e32 v160, 16, v123
	v_and_b32_e32 v161, 0xffff0000, v123
	v_add_f32_e32 v200, v124, v126
	v_add_f32_e32 v200, v200, v128
	v_add_f32_e32 v200, v200, v130
	v_add_f32_e32 v200, v200, v132
	v_add_f32_e32 v200, v200, v134
	v_add_f32_e32 v200, v200, v136
	v_add_f32_e32 v200, v200, v138
	v_add_f32_e32 v200, v200, v140
	v_add_f32_e32 v200, v200, v142
	v_add_f32_e32 v200, v200, v144
	v_add_f32_e32 v200, v200, v146
	v_add_f32_e32 v200, v200, v148
	v_add_f32_e32 v200, v200, v150
	v_add_f32_e32 v200, v200, v152
	v_add_f32_e32 v200, v200, v154
	v_fma_f32 v200, v200, v226, -v154
	v_add_f32_e32 v201, v125, v127
	v_add_f32_e32 v201, v201, v129
	v_add_f32_e32 v201, v201, v131
	v_add_f32_e32 v201, v201, v133
	v_add_f32_e32 v201, v201, v135
	v_add_f32_e32 v201, v201, v137
	v_add_f32_e32 v201, v201, v139
	v_add_f32_e32 v201, v201, v141
	v_add_f32_e32 v201, v201, v143
	v_add_f32_e32 v201, v201, v145
	v_add_f32_e32 v201, v201, v147
	v_add_f32_e32 v201, v201, v149
	v_add_f32_e32 v201, v201, v151
	v_add_f32_e32 v201, v201, v153
	v_add_f32_e32 v201, v201, v155
	v_fma_f32 v201, v201, v226, -v155
	v_add_f32_e32 v208, v126, v128
	v_add_f32_e32 v208, v208, v130
	v_add_f32_e32 v208, v208, v132
	v_add_f32_e32 v208, v208, v134
	v_add_f32_e32 v208, v208, v136
	v_add_f32_e32 v208, v208, v138
	v_add_f32_e32 v208, v208, v140
	v_add_f32_e32 v208, v208, v142
	v_add_f32_e32 v208, v208, v144
	v_add_f32_e32 v208, v208, v146
	v_add_f32_e32 v208, v208, v148
	v_add_f32_e32 v208, v208, v150
	v_add_f32_e32 v208, v208, v152
	v_add_f32_e32 v208, v208, v154
	v_add_f32_e32 v208, v208, v156
	v_fma_f32 v208, v208, v227, -v156
	v_add_f32_e32 v209, v127, v129
	v_add_f32_e32 v209, v209, v131
	v_add_f32_e32 v209, v209, v133
	v_add_f32_e32 v209, v209, v135
	v_add_f32_e32 v209, v209, v137
	v_add_f32_e32 v209, v209, v139
	v_add_f32_e32 v209, v209, v141
	v_add_f32_e32 v209, v209, v143
	v_add_f32_e32 v209, v209, v145
	v_add_f32_e32 v209, v209, v147
	v_add_f32_e32 v209, v209, v149
	v_add_f32_e32 v209, v209, v151
	v_add_f32_e32 v209, v209, v153
	v_add_f32_e32 v209, v209, v155
	v_add_f32_e32 v209, v209, v157
	v_fma_f32 v209, v209, v227, -v157
	v_add_f32_e32 v216, v128, v130
	v_add_f32_e32 v216, v216, v132
	v_add_f32_e32 v216, v216, v134
	v_add_f32_e32 v216, v216, v136
	v_add_f32_e32 v216, v216, v138
	v_add_f32_e32 v216, v216, v140
	v_add_f32_e32 v216, v216, v142
	v_add_f32_e32 v216, v216, v144
	v_add_f32_e32 v216, v216, v146
	v_add_f32_e32 v216, v216, v148
	v_add_f32_e32 v216, v216, v150
	v_add_f32_e32 v216, v216, v152
	v_add_f32_e32 v216, v216, v154
	v_add_f32_e32 v216, v216, v156
	v_add_f32_e32 v216, v216, v158
	v_fma_f32 v216, v216, v228, -v158
	v_add_f32_e32 v217, v129, v131
	v_add_f32_e32 v217, v217, v133
	v_add_f32_e32 v217, v217, v135
	v_add_f32_e32 v217, v217, v137
	v_add_f32_e32 v217, v217, v139
	v_add_f32_e32 v217, v217, v141
	v_add_f32_e32 v217, v217, v143
	v_add_f32_e32 v217, v217, v145
	v_add_f32_e32 v217, v217, v147
	v_add_f32_e32 v217, v217, v149
	v_add_f32_e32 v217, v217, v151
	v_add_f32_e32 v217, v217, v153
	v_add_f32_e32 v217, v217, v155
	v_add_f32_e32 v217, v217, v157
	v_add_f32_e32 v217, v217, v159
	v_fma_f32 v217, v217, v228, -v159
	v_add_f32_e32 v224, v130, v132
	v_add_f32_e32 v224, v224, v134
	v_add_f32_e32 v224, v224, v136
	v_add_f32_e32 v224, v224, v138
	v_add_f32_e32 v224, v224, v140
	v_add_f32_e32 v224, v224, v142
	v_add_f32_e32 v224, v224, v144
	v_add_f32_e32 v224, v224, v146
	v_add_f32_e32 v224, v224, v148
	v_add_f32_e32 v224, v224, v150
	v_add_f32_e32 v224, v224, v152
	v_add_f32_e32 v224, v224, v154
	v_add_f32_e32 v224, v224, v156
	v_add_f32_e32 v224, v224, v158
	v_add_f32_e32 v224, v224, v160
	v_fma_f32 v224, v224, v229, -v160
	v_add_f32_e32 v225, v131, v133
	v_add_f32_e32 v225, v225, v135
	v_add_f32_e32 v225, v225, v137
	v_add_f32_e32 v225, v225, v139
	v_add_f32_e32 v225, v225, v141
	v_add_f32_e32 v225, v225, v143
	v_add_f32_e32 v225, v225, v145
	v_add_f32_e32 v225, v225, v147
	v_add_f32_e32 v225, v225, v149
	v_add_f32_e32 v225, v225, v151
	v_add_f32_e32 v225, v225, v153
	v_add_f32_e32 v225, v225, v155
	v_add_f32_e32 v225, v225, v157
	v_add_f32_e32 v225, v225, v159
	v_add_f32_e32 v225, v225, v161
	v_fma_f32 v225, v225, v229, -v161
	v_cvt_pk_bf16_f32 v194, v194, v195
	v_cvt_pk_bf16_f32 v195, v196, v197
	v_cvt_pk_bf16_f32 v196, v198, v199
	v_cvt_pk_bf16_f32 v197, v200, v201
	global_store_dwordx4 v17, v[194:197], s[14:15]
	v_cvt_pk_bf16_f32 v202, v202, v203
	v_cvt_pk_bf16_f32 v203, v204, v205
	v_cvt_pk_bf16_f32 v204, v206, v207
	v_cvt_pk_bf16_f32 v205, v208, v209
	v_add_u32_e32 v13, 0x800, v17
	global_store_dwordx4 v13, v[202:205], s[14:15]
	v_cvt_pk_bf16_f32 v210, v210, v211
	v_cvt_pk_bf16_f32 v211, v212, v213
	v_cvt_pk_bf16_f32 v212, v214, v215
	v_cvt_pk_bf16_f32 v213, v216, v217
	v_add_u32_e32 v13, 0x1000, v17
	global_store_dwordx4 v13, v[210:213], s[14:15]
	v_cvt_pk_bf16_f32 v218, v218, v219
	v_cvt_pk_bf16_f32 v219, v220, v221
	v_cvt_pk_bf16_f32 v220, v222, v223
	v_cvt_pk_bf16_f32 v221, v224, v225
	v_add_u32_e32 v13, 0x1800, v17
	global_store_dwordx4 v13, v[218:221], s[14:15]
	s_branch .Lpc_conv
; __device__ __forceinline__ unsigned pk2(float lo, float hi) { return pg8::cvt_pk_bf16(lo, hi); }
; __device__ __forceinline__ void unpack8(const v4u w, float (&f)[8]) { f[0] = bflo(w.x); f[1] = bfhi(w.x); f[2] = bflo(w.y); f[3] = bfhi(w.y); f[4] = bflo(w.z); f[5] = bfhi(w.z); f[6] = bflo(w.w); f[7] = bfhi(w.w); }
; template <int W> __device__ __forceinline__ void pool_item(Frame& F, int row, int t, int c8) {
;     float s[8], u[8];
; #pragma unroll
;     for (int i = 0; i < 8; ++i) s[i] = 0.f;
;     v4u ld[W];
; #pragma unroll
;     for (int k = 0; k < W; ++k) { const int kk = (t - k) >= 0 ? k : t; ld[k] = *(const v4u*)(F.PROJ + (size_t)(row - kk) * INWP + O_UPOOL + c8); }
; #pragma unroll
;     for (int k = W - 1; k >= 0; --k) { unpack8(ld[k], u); const float wgt = (t - k) >= 0 ? 1.f : 0.f;
; #pragma unroll
;         for (int i = 0; i < 8; ++i) s[i] += wgt * u[i]; }
;     const int cnt = (t + 1) < W ? (t + 1) : W;
;     const float inv = 1.0f / (float)cnt;
;     v4u o; o.x = pk2(s[0] * inv - u[0], s[1] * inv - u[1]); o.y = pk2(s[2] * inv - u[2], s[3] * inv - u[3]); o.z = pk2(s[4] * inv - u[4], s[5] * inv - u[5]); o.w = pk2(s[6] * inv - u[6], s[7] * inv - u[7]);
;     *(v4u*)(F.Y + (size_t)row * 1024 + c8) = o;
; }
.Lpc_g1:
	v_add_u32_e32 v14, 0x200, v7
	v_add_u32_e32 v15, 0x400, v7
	v_add_u32_e32 v16, 0x200, v9
	v_add_u32_e32 v17, 0x400, v9
	v_min_u32_e32 v11, 0xa200, v6
	v_sub_u32_e32 v12, v14, v11
	global_load_dwordx4 v[20:23], v12, s[96:97]
	v_min_u32_e32 v11, 0x6c00, v6
	v_sub_u32_e32 v12, v14, v11
	global_load_dwordx4 v[24:27], v12, s[96:97]
	v_min_u32_e32 v11, 0x3600, v6
	v_sub_u32_e32 v12, v14, v11
	global_load_dwordx4 v[28:31], v12, s[96:97]
	global_load_dwordx4 v[32:35], v14, s[96:97]
	v_add_u32_e32 v12, 0x3600, v14
	global_load_dwordx4 v[36:39], v12, s[96:97]
	v_add_u32_e32 v12, 0x6c00, v14
	global_load_dwordx4 v[40:43], v12, s[96:97]
	v_add_u32_e32 v12, 0xa200, v14
	global_load_dwordx4 v[44:47], v12, s[96:97]
	v_min_u32_e32 v11, 0x17a00, v6
	v_sub_u32_e32 v12, v15, v11
	global_load_dwordx4 v[48:51], v12, s[96:97]
	v_min_u32_e32 v11, 0x14400, v6
	v_sub_u32_e32 v12, v15, v11
	global_load_dwordx4 v[52:55], v12, s[96:97]
	v_min_u32_e32 v11, 0x10e00, v6
	v_sub_u32_e32 v12, v15, v11
	global_load_dwordx4 v[56:59], v12, s[96:97]
	v_min_u32_e32 v11, 0xd800, v6
	v_sub_u32_e32 v12, v15, v11
	global_load_dwordx4 v[60:63], v12, s[96:97]
	v_min_u32_e32 v11, 0xa200, v6
	v_sub_u32_e32 v12, v15, v11
	global_load_dwordx4 v[64:67], v12, s[96:97]
	v_min_u32_e32 v11, 0x6c00, v6
	v_sub_u32_e32 v12, v15, v11
	global_load_dwordx4 v[68:71], v12, s[96:97]
	v_min_u32_e32 v11, 0x3600, v6
	v_sub_u32_e32 v12, v15, v11
	global_load_dwordx4 v[72:75], v12, s[96:97]
	global_load_dwordx4 v[76:79], v15, s[96:97]
	v_add_u32_e32 v12, 0x3600, v15
	global_load_dwordx4 v[80:83], v12, s[96:97]
	v_add_u32_e32 v12, 0x6c00, v15
	global_load_dwordx4 v[84:87], v12, s[96:97]
	v_add_u32_e32 v12, 0xa200, v15
	global_load_dwordx4 v[88:91], v12, s[96:97]
	s_waitcnt vmcnt(11)
	v_cmp_le_u32_e32 vcc, 3, v5
	s_nop 1
	v_cndmask_b32_e32 v20, 0, v20, vcc
	v_cndmask_b32_e32 v21, 0, v21, vcc
	v_cndmask_b32_e32 v22, 0, v22, vcc
	v_cndmask_b32_e32 v23, 0, v23, vcc
	v_cmp_le_u32_e32 vcc, 2, v5
	s_nop 1
	v_cndmask_b32_e32 v24, 0, v24, vcc
	v_cndmask_b32_e32 v25, 0, v25, vcc
	v_cndmask_b32_e32 v26, 0, v26, vcc
	v_cndmask_b32_e32 v27, 0, v27, vcc
	v_cmp_le_u32_e32 vcc, 1, v5
	s_nop 1
	v_cndmask_b32_e32 v28, 0, v28, vcc
	v_cndmask_b32_e32 v29, 0, v29, vcc
	v_cndmask_b32_e32 v30, 0, v30, vcc
	v_cndmask_b32_e32 v31, 0, v31, vcc
	v_add_u32_e32 v226, 1, v5
	v_min_u32_e32 v226, 4, v226
	v_cvt_f32_u32_e32 v226, v226
	v_rcp_f32_e32 v226, v226
	v_add_u32_e32 v227, 2, v5
	v_min_u32_e32 v227, 4, v227
	v_cvt_f32_u32_e32 v227, v227
	v_rcp_f32_e32 v227, v227
	v_add_u32_e32 v228, 3, v5
	v_min_u32_e32 v228, 4, v228
	v_cvt_f32_u32_e32 v228, v228
	v_rcp_f32_e32 v228, v228
	v_add_u32_e32 v229, 4, v5
	v_min_u32_e32 v229, 4, v229
	v_cvt_f32_u32_e32 v229, v229
	v_rcp_f32_e32 v229, v229
	v_lshlrev_b32_e32 v124, 16, v20
	v_and_b32_e32 v125, 0xffff0000, v20
	v_lshlrev_b32_e32 v126, 16, v24
	v_and_b32_e32 v127, 0xffff0000, v24
	v_lshlrev_b32_e32 v128, 16, v28
	v_and_b32_e32 v129, 0xffff0000, v28
	v_lshlrev_b32_e32 v130, 16, v32
	v_and_b32_e32 v131, 0xffff0000, v32
	v_lshlrev_b32_e32 v132, 16, v36
	v_and_b32_e32 v133, 0xffff0000, v36
	v_lshlrev_b32_e32 v134, 16, v40
	v_and_b32_e32 v135, 0xffff0000, v40
	v_lshlrev_b32_e32 v136, 16, v44
	v_and_b32_e32 v137, 0xffff0000, v44
	v_add_f32_e32 v194, v124, v126
	v_add_f32_e32 v194, v194, v128
	v_add_f32_e32 v194, v194, v130
	v_fma_f32 v194, v194, v226, -v130
	v_add_f32_e32 v195, v125, v127
	v_add_f32_e32 v195, v195, v129
	v_add_f32_e32 v195, v195, v131
	v_fma_f32 v195, v195, v226, -v131
	v_add_f32_e32 v202, v126, v128
	v_add_f32_e32 v202, v202, v130
	v_add_f32_e32 v202, v202, v132
	v_fma_f32 v202, v202, v227, -v132
	v_add_f32_e32 v203, v127, v129
	v_add_f32_e32 v203, v203, v131
	v_add_f32_e32 v203, v203, v133
	v_fma_f32 v203, v203, v227, -v133
	v_add_f32_e32 v210, v128, v130
	v_add_f32_e32 v210, v210, v132
	v_add_f32_e32 v210, v210, v134
	v_fma_f32 v210, v210, v228, -v134
	v_add_f32_e32 v211, v129, v131
	v_add_f32_e32 v211, v211, v133
	v_add_f32_e32 v211, v211, v135
	v_fma_f32 v211, v211, v228, -v135
	v_add_f32_e32 v218, v130, v132
	v_add_f32_e32 v218, v218, v134
	v_add_f32_e32 v218, v218, v136
	v_fma_f32 v218, v218, v229, -v136
	v_add_f32_e32 v219, v131, v133
	v_add_f32_e32 v219, v219, v135
	v_add_f32_e32 v219, v219, v137
	v_fma_f32 v219, v219, v229, -v137
	v_lshlrev_b32_e32 v124, 16, v21
	v_and_b32_e32 v125, 0xffff0000, v21
	v_lshlrev_b32_e32 v126, 16, v25
	v_and_b32_e32 v127, 0xffff0000, v25
	v_lshlrev_b32_e32 v128, 16, v29
	v_and_b32_e32 v129, 0xffff0000, v29
	v_lshlrev_b32_e32 v130, 16, v33
	v_and_b32_e32 v131, 0xffff0000, v33
	v_lshlrev_b32_e32 v132, 16, v37
	v_and_b32_e32 v133, 0xffff0000, v37
	v_lshlrev_b32_e32 v134, 16, v41
	v_and_b32_e32 v135, 0xffff0000, v41
	v_lshlrev_b32_e32 v136, 16, v45
	v_and_b32_e32 v137, 0xffff0000, v45
	v_add_f32_e32 v196, v124, v126
	v_add_f32_e32 v196, v196, v128
	v_add_f32_e32 v196, v196, v130
	v_fma_f32 v196, v196, v226, -v130
	v_add_f32_e32 v197, v125, v127
	v_add_f32_e32 v197, v197, v129
	v_add_f32_e32 v197, v197, v131
	v_fma_f32 v197, v197, v226, -v131
	v_add_f32_e32 v204, v126, v128
	v_add_f32_e32 v204, v204, v130
	v_add_f32_e32 v204, v204, v132
	v_fma_f32 v204, v204, v227, -v132
	v_add_f32_e32 v205, v127, v129
	v_add_f32_e32 v205, v205, v131
	v_add_f32_e32 v205, v205, v133
	v_fma_f32 v205, v205, v227, -v133
	v_add_f32_e32 v212, v128, v130
	v_add_f32_e32 v212, v212, v132
	v_add_f32_e32 v212, v212, v134
	v_fma_f32 v212, v212, v228, -v134
	v_add_f32_e32 v213, v129, v131
	v_add_f32_e32 v213, v213, v133
	v_add_f32_e32 v213, v213, v135
	v_fma_f32 v213, v213, v228, -v135
	v_add_f32_e32 v220, v130, v132
	v_add_f32_e32 v220, v220, v134
; __device__ __forceinline__ unsigned pk2(float lo, float hi) { return pg8::cvt_pk_bf16(lo, hi); }
; __device__ __forceinline__ void unpack8(const v4u w, float (&f)[8]) { f[0] = bflo(w.x); f[1] = bfhi(w.x); f[2] = bflo(w.y); f[3] = bfhi(w.y); f[4] = bflo(w.z); f[5] = bfhi(w.z); f[6] = bflo(w.w); f[7] = bfhi(w.w); }
; template <int W> __device__ __forceinline__ void pool_item(Frame& F, int row, int t, int c8) {
;     float s[8], u[8];
; #pragma unroll
;     for (int i = 0; i < 8; ++i) s[i] = 0.f;
;     v4u ld[W];
; #pragma unroll
;     for (int k = 0; k < W; ++k) { const int kk = (t - k) >= 0 ? k : t; ld[k] = *(const v4u*)(F.PROJ + (size_t)(row - kk) * INWP + O_UPOOL + c8); }
; #pragma unroll
;     for (int k = W - 1; k >= 0; --k) { unpack8(ld[k], u); const float wgt = (t - k) >= 0 ? 1.f : 0.f;
; #pragma unroll
;         for (int i = 0; i < 8; ++i) s[i] += wgt * u[i]; }
;     const int cnt = (t + 1) < W ? (t + 1) : W;
;     const float inv = 1.0f / (float)cnt;
;     v4u o; o.x = pk2(s[0] * inv - u[0], s[1] * inv - u[1]); o.y = pk2(s[2] * inv - u[2], s[3] * inv - u[3]); o.z = pk2(s[4] * inv - u[4], s[5] * inv - u[5]); o.w = pk2(s[6] * inv - u[6], s[7] * inv - u[7]);
;     *(v4u*)(F.Y + (size_t)row * 1024 + c8) = o;
; }
	v_add_f32_e32 v220, v220, v136
	v_fma_f32 v220, v220, v229, -v136
	v_add_f32_e32 v221, v131, v133
	v_add_f32_e32 v221, v221, v135
	v_add_f32_e32 v221, v221, v137
	v_fma_f32 v221, v221, v229, -v137
	v_lshlrev_b32_e32 v124, 16, v22
	v_and_b32_e32 v125, 0xffff0000, v22
	v_lshlrev_b32_e32 v126, 16, v26
	v_and_b32_e32 v127, 0xffff0000, v26
	v_lshlrev_b32_e32 v128, 16, v30
	v_and_b32_e32 v129, 0xffff0000, v30
	v_lshlrev_b32_e32 v130, 16, v34
	v_and_b32_e32 v131, 0xffff0000, v34
	v_lshlrev_b32_e32 v132, 16, v38
	v_and_b32_e32 v133, 0xffff0000, v38
	v_lshlrev_b32_e32 v134, 16, v42
	v_and_b32_e32 v135, 0xffff0000, v42
	v_lshlrev_b32_e32 v136, 16, v46
	v_and_b32_e32 v137, 0xffff0000, v46
	v_add_f32_e32 v198, v124, v126
	v_add_f32_e32 v198, v198, v128
	v_add_f32_e32 v198, v198, v130
	v_fma_f32 v198, v198, v226, -v130
	v_add_f32_e32 v199, v125, v127
	v_add_f32_e32 v199, v199, v129
	v_add_f32_e32 v199, v199, v131
	v_fma_f32 v199, v199, v226, -v131
	v_add_f32_e32 v206, v126, v128
	v_add_f32_e32 v206, v206, v130
	v_add_f32_e32 v206, v206, v132
	v_fma_f32 v206, v206, v227, -v132
	v_add_f32_e32 v207, v127, v129
	v_add_f32_e32 v207, v207, v131
	v_add_f32_e32 v207, v207, v133
	v_fma_f32 v207, v207, v227, -v133
	v_add_f32_e32 v214, v128, v130
	v_add_f32_e32 v214, v214, v132
	v_add_f32_e32 v214, v214, v134
	v_fma_f32 v214, v214, v228, -v134
	v_add_f32_e32 v215, v129, v131
	v_add_f32_e32 v215, v215, v133
	v_add_f32_e32 v215, v215, v135
	v_fma_f32 v215, v215, v228, -v135
	v_add_f32_e32 v222, v130, v132
	v_add_f32_e32 v222, v222, v134
	v_add_f32_e32 v222, v222, v136
	v_fma_f32 v222, v222, v229, -v136
	v_add_f32_e32 v223, v131, v133
	v_add_f32_e32 v223, v223, v135
	v_add_f32_e32 v223, v223, v137
	v_fma_f32 v223, v223, v229, -v137
	v_lshlrev_b32_e32 v124, 16, v23
	v_and_b32_e32 v125, 0xffff0000, v23
	v_lshlrev_b32_e32 v126, 16, v27
	v_and_b32_e32 v127, 0xffff0000, v27
	v_lshlrev_b32_e32 v128, 16, v31
	v_and_b32_e32 v129, 0xffff0000, v31
	v_lshlrev_b32_e32 v130, 16, v35
	v_and_b32_e32 v131, 0xffff0000, v35
	v_lshlrev_b32_e32 v132, 16, v39
	v_and_b32_e32 v133, 0xffff0000, v39
	v_lshlrev_b32_e32 v134, 16, v43
	v_and_b32_e32 v135, 0xffff0000, v43
	v_lshlrev_b32_e32 v136, 16, v47
	v_and_b32_e32 v137, 0xffff0000, v47
	v_add_f32_e32 v200, v124, v126
	v_add_f32_e32 v200, v200, v128
	v_add_f32_e32 v200, v200, v130
	v_fma_f32 v200, v200, v226, -v130
	v_add_f32_e32 v201, v125, v127
	v_add_f32_e32 v201, v201, v129
	v_add_f32_e32 v201, v201, v131
	v_fma_f32 v201, v201, v226, -v131
	v_add_f32_e32 v208, v126, v128
	v_add_f32_e32 v208, v208, v130
	v_add_f32_e32 v208, v208, v132
	v_fma_f32 v208, v208, v227, -v132
	v_add_f32_e32 v209, v127, v129
	v_add_f32_e32 v209, v209, v131
	v_add_f32_e32 v209, v209, v133
	v_fma_f32 v209, v209, v227, -v133
	v_add_f32_e32 v216, v128, v130
	v_add_f32_e32 v216, v216, v132
	v_add_f32_e32 v216, v216, v134
	v_fma_f32 v216, v216, v228, -v134
	v_add_f32_e32 v217, v129, v131
	v_add_f32_e32 v217, v217, v133
	v_add_f32_e32 v217, v217, v135
	v_fma_f32 v217, v217, v228, -v135
	v_add_f32_e32 v224, v130, v132
	v_add_f32_e32 v224, v224, v134
	v_add_f32_e32 v224, v224, v136
	v_fma_f32 v224, v224, v229, -v136
	v_add_f32_e32 v225, v131, v133
	v_add_f32_e32 v225, v225, v135
	v_add_f32_e32 v225, v225, v137
	v_fma_f32 v225, v225, v229, -v137
	v_cvt_pk_bf16_f32 v194, v194, v195
	v_cvt_pk_bf16_f32 v195, v196, v197
	v_cvt_pk_bf16_f32 v196, v198, v199
	v_cvt_pk_bf16_f32 v197, v200, v201
	global_store_dwordx4 v16, v[194:197], s[14:15]
	v_cvt_pk_bf16_f32 v202, v202, v203
	v_cvt_pk_bf16_f32 v203, v204, v205
	v_cvt_pk_bf16_f32 v204, v206, v207
	v_cvt_pk_bf16_f32 v205, v208, v209
	v_add_u32_e32 v13, 0x800, v16
	global_store_dwordx4 v13, v[202:205], s[14:15]
	v_cvt_pk_bf16_f32 v210, v210, v211
	v_cvt_pk_bf16_f32 v211, v212, v213
	v_cvt_pk_bf16_f32 v212, v214, v215
	v_cvt_pk_bf16_f32 v213, v216, v217
	v_add_u32_e32 v13, 0x1000, v16
	global_store_dwordx4 v13, v[210:213], s[14:15]
	v_cvt_pk_bf16_f32 v218, v218, v219
	v_cvt_pk_bf16_f32 v219, v220, v221
	v_cvt_pk_bf16_f32 v220, v222, v223
	v_cvt_pk_bf16_f32 v221, v224, v225
	v_add_u32_e32 v13, 0x1800, v16
	global_store_dwordx4 v13, v[218:221], s[14:15]
	s_waitcnt vmcnt(4)
	v_cmp_le_u32_e32 vcc, 7, v5
	s_nop 1
	v_cndmask_b32_e32 v48, 0, v48, vcc
	v_cndmask_b32_e32 v49, 0, v49, vcc
	v_cndmask_b32_e32 v50, 0, v50, vcc
	v_cndmask_b32_e32 v51, 0, v51, vcc
	v_cmp_le_u32_e32 vcc, 6, v5
	s_nop 1
	v_cndmask_b32_e32 v52, 0, v52, vcc
	v_cndmask_b32_e32 v53, 0, v53, vcc
	v_cndmask_b32_e32 v54, 0, v54, vcc
	v_cndmask_b32_e32 v55, 0, v55, vcc
	v_cmp_le_u32_e32 vcc, 5, v5
	s_nop 1
	v_cndmask_b32_e32 v56, 0, v56, vcc
	v_cndmask_b32_e32 v57, 0, v57, vcc
	v_cndmask_b32_e32 v58, 0, v58, vcc
	v_cndmask_b32_e32 v59, 0, v59, vcc
	v_cmp_le_u32_e32 vcc, 4, v5
	s_nop 1
	v_cndmask_b32_e32 v60, 0, v60, vcc
	v_cndmask_b32_e32 v61, 0, v61, vcc
	v_cndmask_b32_e32 v62, 0, v62, vcc
	v_cndmask_b32_e32 v63, 0, v63, vcc
	v_cmp_le_u32_e32 vcc, 3, v5
	s_nop 1
	v_cndmask_b32_e32 v64, 0, v64, vcc
	v_cndmask_b32_e32 v65, 0, v65, vcc
	v_cndmask_b32_e32 v66, 0, v66, vcc
	v_cndmask_b32_e32 v67, 0, v67, vcc
	v_cmp_le_u32_e32 vcc, 2, v5
	s_nop 1
	v_cndmask_b32_e32 v68, 0, v68, vcc
	v_cndmask_b32_e32 v69, 0, v69, vcc
	v_cndmask_b32_e32 v70, 0, v70, vcc
	v_cndmask_b32_e32 v71, 0, v71, vcc
	v_cmp_le_u32_e32 vcc, 1, v5
	s_nop 1
	v_cndmask_b32_e32 v72, 0, v72, vcc
	v_cndmask_b32_e32 v73, 0, v73, vcc
	v_cndmask_b32_e32 v74, 0, v74, vcc
	v_cndmask_b32_e32 v75, 0, v75, vcc
	v_add_u32_e32 v226, 1, v5
	v_min_u32_e32 v226, 8, v226
	v_cvt_f32_u32_e32 v226, v226
	v_rcp_f32_e32 v226, v226
	v_add_u32_e32 v227, 2, v5
	v_min_u32_e32 v227, 8, v227
	v_cvt_f32_u32_e32 v227, v227
; __device__ __forceinline__ unsigned pk2(float lo, float hi) { return pg8::cvt_pk_bf16(lo, hi); }
; __device__ __forceinline__ void unpack8(const v4u w, float (&f)[8]) { f[0] = bflo(w.x); f[1] = bfhi(w.x); f[2] = bflo(w.y); f[3] = bfhi(w.y); f[4] = bflo(w.z); f[5] = bfhi(w.z); f[6] = bflo(w.w); f[7] = bfhi(w.w); }
; template <int W> __device__ __forceinline__ void pool_item(Frame& F, int row, int t, int c8) {
;     float s[8], u[8];
; #pragma unroll
;     for (int i = 0; i < 8; ++i) s[i] = 0.f;
;     v4u ld[W];
; #pragma unroll
;     for (int k = 0; k < W; ++k) { const int kk = (t - k) >= 0 ? k : t; ld[k] = *(const v4u*)(F.PROJ + (size_t)(row - kk) * INWP + O_UPOOL + c8); }
; #pragma unroll
;     for (int k = W - 1; k >= 0; --k) { unpack8(ld[k], u); const float wgt = (t - k) >= 0 ? 1.f : 0.f;
; #pragma unroll
;         for (int i = 0; i < 8; ++i) s[i] += wgt * u[i]; }
;     const int cnt = (t + 1) < W ? (t + 1) : W;
;     const float inv = 1.0f / (float)cnt;
;     v4u o; o.x = pk2(s[0] * inv - u[0], s[1] * inv - u[1]); o.y = pk2(s[2] * inv - u[2], s[3] * inv - u[3]); o.z = pk2(s[4] * inv - u[4], s[5] * inv - u[5]); o.w = pk2(s[6] * inv - u[6], s[7] * inv - u[7]);
;     *(v4u*)(F.Y + (size_t)row * 1024 + c8) = o;
; }
	v_rcp_f32_e32 v227, v227
	v_add_u32_e32 v228, 3, v5
	v_min_u32_e32 v228, 8, v228
	v_cvt_f32_u32_e32 v228, v228
	v_rcp_f32_e32 v228, v228
	v_add_u32_e32 v229, 4, v5
	v_min_u32_e32 v229, 8, v229
	v_cvt_f32_u32_e32 v229, v229
	v_rcp_f32_e32 v229, v229
	v_lshlrev_b32_e32 v124, 16, v48
	v_and_b32_e32 v125, 0xffff0000, v48
	v_lshlrev_b32_e32 v126, 16, v52
	v_and_b32_e32 v127, 0xffff0000, v52
	v_lshlrev_b32_e32 v128, 16, v56
	v_and_b32_e32 v129, 0xffff0000, v56
	v_lshlrev_b32_e32 v130, 16, v60
	v_and_b32_e32 v131, 0xffff0000, v60
	v_lshlrev_b32_e32 v132, 16, v64
	v_and_b32_e32 v133, 0xffff0000, v64
	v_lshlrev_b32_e32 v134, 16, v68
	v_and_b32_e32 v135, 0xffff0000, v68
	v_lshlrev_b32_e32 v136, 16, v72
	v_and_b32_e32 v137, 0xffff0000, v72
	v_lshlrev_b32_e32 v138, 16, v76
	v_and_b32_e32 v139, 0xffff0000, v76
	v_lshlrev_b32_e32 v140, 16, v80
	v_and_b32_e32 v141, 0xffff0000, v80
	v_lshlrev_b32_e32 v142, 16, v84
	v_and_b32_e32 v143, 0xffff0000, v84
	v_lshlrev_b32_e32 v144, 16, v88
	v_and_b32_e32 v145, 0xffff0000, v88
	v_add_f32_e32 v194, v124, v126
	v_add_f32_e32 v194, v194, v128
	v_add_f32_e32 v194, v194, v130
	v_add_f32_e32 v194, v194, v132
	v_add_f32_e32 v194, v194, v134
	v_add_f32_e32 v194, v194, v136
	v_add_f32_e32 v194, v194, v138
	v_fma_f32 v194, v194, v226, -v138
	v_add_f32_e32 v195, v125, v127
	v_add_f32_e32 v195, v195, v129
	v_add_f32_e32 v195, v195, v131
	v_add_f32_e32 v195, v195, v133
	v_add_f32_e32 v195, v195, v135
	v_add_f32_e32 v195, v195, v137
	v_add_f32_e32 v195, v195, v139
	v_fma_f32 v195, v195, v226, -v139
	v_add_f32_e32 v202, v126, v128
	v_add_f32_e32 v202, v202, v130
	v_add_f32_e32 v202, v202, v132
	v_add_f32_e32 v202, v202, v134
	v_add_f32_e32 v202, v202, v136
	v_add_f32_e32 v202, v202, v138
	v_add_f32_e32 v202, v202, v140
	v_fma_f32 v202, v202, v227, -v140
	v_add_f32_e32 v203, v127, v129
	v_add_f32_e32 v203, v203, v131
	v_add_f32_e32 v203, v203, v133
	v_add_f32_e32 v203, v203, v135
	v_add_f32_e32 v203, v203, v137
	v_add_f32_e32 v203, v203, v139
	v_add_f32_e32 v203, v203, v141
	v_fma_f32 v203, v203, v227, -v141
	v_add_f32_e32 v210, v128, v130
	v_add_f32_e32 v210, v210, v132
	v_add_f32_e32 v210, v210, v134
	v_add_f32_e32 v210, v210, v136
	v_add_f32_e32 v210, v210, v138
	v_add_f32_e32 v210, v210, v140
	v_add_f32_e32 v210, v210, v142
	v_fma_f32 v210, v210, v228, -v142
	v_add_f32_e32 v211, v129, v131
	v_add_f32_e32 v211, v211, v133
	v_add_f32_e32 v211, v211, v135
	v_add_f32_e32 v211, v211, v137
	v_add_f32_e32 v211, v211, v139
	v_add_f32_e32 v211, v211, v141
	v_add_f32_e32 v211, v211, v143
	v_fma_f32 v211, v211, v228, -v143
	v_add_f32_e32 v218, v130, v132
	v_add_f32_e32 v218, v218, v134
	v_add_f32_e32 v218, v218, v136
	v_add_f32_e32 v218, v218, v138
	v_add_f32_e32 v218, v218, v140
	v_add_f32_e32 v218, v218, v142
	v_add_f32_e32 v218, v218, v144
	v_fma_f32 v218, v218, v229, -v144
	v_add_f32_e32 v219, v131, v133
	v_add_f32_e32 v219, v219, v135
	v_add_f32_e32 v219, v219, v137
	v_add_f32_e32 v219, v219, v139
	v_add_f32_e32 v219, v219, v141
	v_add_f32_e32 v219, v219, v143
	v_add_f32_e32 v219, v219, v145
	v_fma_f32 v219, v219, v229, -v145
	v_lshlrev_b32_e32 v124, 16, v49
	v_and_b32_e32 v125, 0xffff0000, v49
	v_lshlrev_b32_e32 v126, 16, v53
	v_and_b32_e32 v127, 0xffff0000, v53
	v_lshlrev_b32_e32 v128, 16, v57
	v_and_b32_e32 v129, 0xffff0000, v57
	v_lshlrev_b32_e32 v130, 16, v61
	v_and_b32_e32 v131, 0xffff0000, v61
	v_lshlrev_b32_e32 v132, 16, v65
	v_and_b32_e32 v133, 0xffff0000, v65
	v_lshlrev_b32_e32 v134, 16, v69
	v_and_b32_e32 v135, 0xffff0000, v69
	v_lshlrev_b32_e32 v136, 16, v73
	v_and_b32_e32 v137, 0xffff0000, v73
	v_lshlrev_b32_e32 v138, 16, v77
	v_and_b32_e32 v139, 0xffff0000, v77
	v_lshlrev_b32_e32 v140, 16, v81
	v_and_b32_e32 v141, 0xffff0000, v81
	v_lshlrev_b32_e32 v142, 16, v85
	v_and_b32_e32 v143, 0xffff0000, v85
	v_lshlrev_b32_e32 v144, 16, v89
	v_and_b32_e32 v145, 0xffff0000, v89
	v_add_f32_e32 v196, v124, v126
	v_add_f32_e32 v196, v196, v128
	v_add_f32_e32 v196, v196, v130
	v_add_f32_e32 v196, v196, v132
	v_add_f32_e32 v196, v196, v134
	v_add_f32_e32 v196, v196, v136
	v_add_f32_e32 v196, v196, v138
	v_fma_f32 v196, v196, v226, -v138
	v_add_f32_e32 v197, v125, v127
	v_add_f32_e32 v197, v197, v129
	v_add_f32_e32 v197, v197, v131
	v_add_f32_e32 v197, v197, v133
	v_add_f32_e32 v197, v197, v135
	v_add_f32_e32 v197, v197, v137
	v_add_f32_e32 v197, v197, v139
	v_fma_f32 v197, v197, v226, -v139
	v_add_f32_e32 v204, v126, v128
	v_add_f32_e32 v204, v204, v130
	v_add_f32_e32 v204, v204, v132
	v_add_f32_e32 v204, v204, v134
	v_add_f32_e32 v204, v204, v136
	v_add_f32_e32 v204, v204, v138
	v_add_f32_e32 v204, v204, v140
	v_fma_f32 v204, v204, v227, -v140
	v_add_f32_e32 v205, v127, v129
	v_add_f32_e32 v205, v205, v131
	v_add_f32_e32 v205, v205, v133
	v_add_f32_e32 v205, v205, v135
	v_add_f32_e32 v205, v205, v137
	v_add_f32_e32 v205, v205, v139
	v_add_f32_e32 v205, v205, v141
	v_fma_f32 v205, v205, v227, -v141
	v_add_f32_e32 v212, v128, v130
	v_add_f32_e32 v212, v212, v132
	v_add_f32_e32 v212, v212, v134
	v_add_f32_e32 v212, v212, v136
	v_add_f32_e32 v212, v212, v138
	v_add_f32_e32 v212, v212, v140
	v_add_f32_e32 v212, v212, v142
	v_fma_f32 v212, v212, v228, -v142
	v_add_f32_e32 v213, v129, v131
	v_add_f32_e32 v213, v213, v133
	v_add_f32_e32 v213, v213, v135
	v_add_f32_e32 v213, v213, v137
	v_add_f32_e32 v213, v213, v139
	v_add_f32_e32 v213, v213, v141
	v_add_f32_e32 v213, v213, v143
	v_fma_f32 v213, v213, v228, -v143
	v_add_f32_e32 v220, v130, v132
	v_add_f32_e32 v220, v220, v134
	v_add_f32_e32 v220, v220, v136
	v_add_f32_e32 v220, v220, v138
	v_add_f32_e32 v220, v220, v140
	v_add_f32_e32 v220, v220, v142
	v_add_f32_e32 v220, v220, v144
; __device__ __forceinline__ unsigned pk2(float lo, float hi) { return pg8::cvt_pk_bf16(lo, hi); }
; __device__ __forceinline__ void unpack8(const v4u w, float (&f)[8]) { f[0] = bflo(w.x); f[1] = bfhi(w.x); f[2] = bflo(w.y); f[3] = bfhi(w.y); f[4] = bflo(w.z); f[5] = bfhi(w.z); f[6] = bflo(w.w); f[7] = bfhi(w.w); }
; template <int W> __device__ __forceinline__ void pool_item(Frame& F, int row, int t, int c8) {
;     float s[8], u[8];
; #pragma unroll
;     for (int i = 0; i < 8; ++i) s[i] = 0.f;
;     v4u ld[W];
; #pragma unroll
;     for (int k = 0; k < W; ++k) { const int kk = (t - k) >= 0 ? k : t; ld[k] = *(const v4u*)(F.PROJ + (size_t)(row - kk) * INWP + O_UPOOL + c8); }
; #pragma unroll
;     for (int k = W - 1; k >= 0; --k) { unpack8(ld[k], u); const float wgt = (t - k) >= 0 ? 1.f : 0.f;
; #pragma unroll
;         for (int i = 0; i < 8; ++i) s[i] += wgt * u[i]; }
;     const int cnt = (t + 1) < W ? (t + 1) : W;
;     const float inv = 1.0f / (float)cnt;
;     v4u o; o.x = pk2(s[0] * inv - u[0], s[1] * inv - u[1]); o.y = pk2(s[2] * inv - u[2], s[3] * inv - u[3]); o.z = pk2(s[4] * inv - u[4], s[5] * inv - u[5]); o.w = pk2(s[6] * inv - u[6], s[7] * inv - u[7]);
;     *(v4u*)(F.Y + (size_t)row * 1024 + c8) = o;
; }
	v_fma_f32 v220, v220, v229, -v144
	v_add_f32_e32 v221, v131, v133
	v_add_f32_e32 v221, v221, v135
	v_add_f32_e32 v221, v221, v137
	v_add_f32_e32 v221, v221, v139
	v_add_f32_e32 v221, v221, v141
	v_add_f32_e32 v221, v221, v143
	v_add_f32_e32 v221, v221, v145
	v_fma_f32 v221, v221, v229, -v145
	v_lshlrev_b32_e32 v124, 16, v50
	v_and_b32_e32 v125, 0xffff0000, v50
	v_lshlrev_b32_e32 v126, 16, v54
	v_and_b32_e32 v127, 0xffff0000, v54
	v_lshlrev_b32_e32 v128, 16, v58
	v_and_b32_e32 v129, 0xffff0000, v58
	v_lshlrev_b32_e32 v130, 16, v62
	v_and_b32_e32 v131, 0xffff0000, v62
	v_lshlrev_b32_e32 v132, 16, v66
	v_and_b32_e32 v133, 0xffff0000, v66
	v_lshlrev_b32_e32 v134, 16, v70
	v_and_b32_e32 v135, 0xffff0000, v70
	v_lshlrev_b32_e32 v136, 16, v74
	v_and_b32_e32 v137, 0xffff0000, v74
	v_lshlrev_b32_e32 v138, 16, v78
	v_and_b32_e32 v139, 0xffff0000, v78
	v_lshlrev_b32_e32 v140, 16, v82
	v_and_b32_e32 v141, 0xffff0000, v82
	v_lshlrev_b32_e32 v142, 16, v86
	v_and_b32_e32 v143, 0xffff0000, v86
	v_lshlrev_b32_e32 v144, 16, v90
	v_and_b32_e32 v145, 0xffff0000, v90
	v_add_f32_e32 v198, v124, v126
	v_add_f32_e32 v198, v198, v128
	v_add_f32_e32 v198, v198, v130
	v_add_f32_e32 v198, v198, v132
	v_add_f32_e32 v198, v198, v134
	v_add_f32_e32 v198, v198, v136
	v_add_f32_e32 v198, v198, v138
	v_fma_f32 v198, v198, v226, -v138
	v_add_f32_e32 v199, v125, v127
	v_add_f32_e32 v199, v199, v129
	v_add_f32_e32 v199, v199, v131
	v_add_f32_e32 v199, v199, v133
	v_add_f32_e32 v199, v199, v135
	v_add_f32_e32 v199, v199, v137
	v_add_f32_e32 v199, v199, v139
	v_fma_f32 v199, v199, v226, -v139
	v_add_f32_e32 v206, v126, v128
	v_add_f32_e32 v206, v206, v130
	v_add_f32_e32 v206, v206, v132
	v_add_f32_e32 v206, v206, v134
	v_add_f32_e32 v206, v206, v136
	v_add_f32_e32 v206, v206, v138
	v_add_f32_e32 v206, v206, v140
	v_fma_f32 v206, v206, v227, -v140
	v_add_f32_e32 v207, v127, v129
	v_add_f32_e32 v207, v207, v131
	v_add_f32_e32 v207, v207, v133
	v_add_f32_e32 v207, v207, v135
	v_add_f32_e32 v207, v207, v137
	v_add_f32_e32 v207, v207, v139
	v_add_f32_e32 v207, v207, v141
	v_fma_f32 v207, v207, v227, -v141
	v_add_f32_e32 v214, v128, v130
	v_add_f32_e32 v214, v214, v132
	v_add_f32_e32 v214, v214, v134
	v_add_f32_e32 v214, v214, v136
	v_add_f32_e32 v214, v214, v138
	v_add_f32_e32 v214, v214, v140
	v_add_f32_e32 v214, v214, v142
	v_fma_f32 v214, v214, v228, -v142
	v_add_f32_e32 v215, v129, v131
	v_add_f32_e32 v215, v215, v133
	v_add_f32_e32 v215, v215, v135
	v_add_f32_e32 v215, v215, v137
	v_add_f32_e32 v215, v215, v139
	v_add_f32_e32 v215, v215, v141
	v_add_f32_e32 v215, v215, v143
	v_fma_f32 v215, v215, v228, -v143
	v_add_f32_e32 v222, v130, v132
	v_add_f32_e32 v222, v222, v134
	v_add_f32_e32 v222, v222, v136
	v_add_f32_e32 v222, v222, v138
	v_add_f32_e32 v222, v222, v140
	v_add_f32_e32 v222, v222, v142
	v_add_f32_e32 v222, v222, v144
	v_fma_f32 v222, v222, v229, -v144
	v_add_f32_e32 v223, v131, v133
	v_add_f32_e32 v223, v223, v135
	v_add_f32_e32 v223, v223, v137
	v_add_f32_e32 v223, v223, v139
	v_add_f32_e32 v223, v223, v141
	v_add_f32_e32 v223, v223, v143
	v_add_f32_e32 v223, v223, v145
	v_fma_f32 v223, v223, v229, -v145
	v_lshlrev_b32_e32 v124, 16, v51
	v_and_b32_e32 v125, 0xffff0000, v51
	v_lshlrev_b32_e32 v126, 16, v55
	v_and_b32_e32 v127, 0xffff0000, v55
	v_lshlrev_b32_e32 v128, 16, v59
	v_and_b32_e32 v129, 0xffff0000, v59
	v_lshlrev_b32_e32 v130, 16, v63
	v_and_b32_e32 v131, 0xffff0000, v63
	v_lshlrev_b32_e32 v132, 16, v67
	v_and_b32_e32 v133, 0xffff0000, v67
	v_lshlrev_b32_e32 v134, 16, v71
	v_and_b32_e32 v135, 0xffff0000, v71
	v_lshlrev_b32_e32 v136, 16, v75
	v_and_b32_e32 v137, 0xffff0000, v75
	v_lshlrev_b32_e32 v138, 16, v79
	v_and_b32_e32 v139, 0xffff0000, v79
	v_lshlrev_b32_e32 v140, 16, v83
	v_and_b32_e32 v141, 0xffff0000, v83
	v_lshlrev_b32_e32 v142, 16, v87
	v_and_b32_e32 v143, 0xffff0000, v87
	v_lshlrev_b32_e32 v144, 16, v91
	v_and_b32_e32 v145, 0xffff0000, v91
	v_add_f32_e32 v200, v124, v126
	v_add_f32_e32 v200, v200, v128
	v_add_f32_e32 v200, v200, v130
	v_add_f32_e32 v200, v200, v132
	v_add_f32_e32 v200, v200, v134
	v_add_f32_e32 v200, v200, v136
	v_add_f32_e32 v200, v200, v138
	v_fma_f32 v200, v200, v226, -v138
	v_add_f32_e32 v201, v125, v127
	v_add_f32_e32 v201, v201, v129
	v_add_f32_e32 v201, v201, v131
	v_add_f32_e32 v201, v201, v133
	v_add_f32_e32 v201, v201, v135
	v_add_f32_e32 v201, v201, v137
	v_add_f32_e32 v201, v201, v139
	v_fma_f32 v201, v201, v226, -v139
	v_add_f32_e32 v208, v126, v128
	v_add_f32_e32 v208, v208, v130
	v_add_f32_e32 v208, v208, v132
	v_add_f32_e32 v208, v208, v134
	v_add_f32_e32 v208, v208, v136
	v_add_f32_e32 v208, v208, v138
	v_add_f32_e32 v208, v208, v140
	v_fma_f32 v208, v208, v227, -v140
	v_add_f32_e32 v209, v127, v129
	v_add_f32_e32 v209, v209, v131
	v_add_f32_e32 v209, v209, v133
	v_add_f32_e32 v209, v209, v135
	v_add_f32_e32 v209, v209, v137
	v_add_f32_e32 v209, v209, v139
	v_add_f32_e32 v209, v209, v141
	v_fma_f32 v209, v209, v227, -v141
	v_add_f32_e32 v216, v128, v130
	v_add_f32_e32 v216, v216, v132
	v_add_f32_e32 v216, v216, v134
	v_add_f32_e32 v216, v216, v136
	v_add_f32_e32 v216, v216, v138
	v_add_f32_e32 v216, v216, v140
	v_add_f32_e32 v216, v216, v142
	v_fma_f32 v216, v216, v228, -v142
	v_add_f32_e32 v217, v129, v131
	v_add_f32_e32 v217, v217, v133
	v_add_f32_e32 v217, v217, v135
	v_add_f32_e32 v217, v217, v137
	v_add_f32_e32 v217, v217, v139
	v_add_f32_e32 v217, v217, v141
	v_add_f32_e32 v217, v217, v143
	v_fma_f32 v217, v217, v228, -v143
	v_add_f32_e32 v224, v130, v132
	v_add_f32_e32 v224, v224, v134
	v_add_f32_e32 v224, v224, v136
	v_add_f32_e32 v224, v224, v138
	v_add_f32_e32 v224, v224, v140
	v_add_f32_e32 v224, v224, v142
	v_add_f32_e32 v224, v224, v144
	v_fma_f32 v224, v224, v229, -v144
	v_add_f32_e32 v225, v131, v133
	v_add_f32_e32 v225, v225, v135
	v_add_f32_e32 v225, v225, v137
	v_add_f32_e32 v225, v225, v139
	v_add_f32_e32 v225, v225, v141
	v_add_f32_e32 v225, v225, v143
	v_add_f32_e32 v225, v225, v145
	v_fma_f32 v225, v225, v229, -v145
	v_cvt_pk_bf16_f32 v194, v194, v195
	v_cvt_pk_bf16_f32 v195, v196, v197
	v_cvt_pk_bf16_f32 v196, v198, v199
	v_cvt_pk_bf16_f32 v197, v200, v201
	global_store_dwordx4 v17, v[194:197], s[14:15]
	v_cvt_pk_bf16_f32 v202, v202, v203
	v_cvt_pk_bf16_f32 v203, v204, v205
	v_cvt_pk_bf16_f32 v204, v206, v207
	v_cvt_pk_bf16_f32 v205, v208, v209
	v_add_u32_e32 v13, 0x800, v17
	global_store_dwordx4 v13, v[202:205], s[14:15]
	v_cvt_pk_bf16_f32 v210, v210, v211
	v_cvt_pk_bf16_f32 v211, v212, v213
	v_cvt_pk_bf16_f32 v212, v214, v215
	v_cvt_pk_bf16_f32 v213, v216, v217
	v_add_u32_e32 v13, 0x1000, v17
	global_store_dwordx4 v13, v[210:213], s[14:15]
	v_cvt_pk_bf16_f32 v218, v218, v219
	v_cvt_pk_bf16_f32 v219, v220, v221
	v_cvt_pk_bf16_f32 v220, v222, v223
	v_cvt_pk_bf16_f32 v221, v224, v225
	v_add_u32_e32 v13, 0x1800, v17
	global_store_dwordx4 v13, v[218:221], s[14:15]
; __device__ __forceinline__ unsigned pk2(float lo, float hi) { return pg8::cvt_pk_bf16(lo, hi); }
; __device__ __forceinline__ void unpack8(const v4u w, float (&f)[8]) { f[0] = bflo(w.x); f[1] = bfhi(w.x); f[2] = bflo(w.y); f[3] = bfhi(w.y); f[4] = bflo(w.z); f[5] = bfhi(w.z); f[6] = bflo(w.w); f[7] = bfhi(w.w); }
; __device__ __forceinline__ void poolconv_phase(Frame& F, const float* conv_w_l) {
;     ...
;     for (int idx = gt; idx < M * 128; idx += NGT) {
;         const int row = idx >> 7, c8 = (idx & 127) * 8, t = row & (SEQ - 1);
;         float acc[8], a[8], b[8];
; #pragma unroll
;         for (int i = 0; i < 8; ++i) acc[i] = 0.f;
;         v4u la[3], lb[3];
; #pragma unroll
;         for (int j = 0; j < 3; ++j) { const int back = (t - 2 + j) >= 0 ? (2 - j) : 0; const bf16* pr = F.PROJ + (size_t)(row - back) * INWP; la[j] = *(const v4u*)(pr + O_CG + c8); lb[j] = *(const v4u*)(pr + O_UCONV + c8); }
;         const v4u lg = *(const v4u*)(F.PROJ + (size_t)row * INWP + O_BG + c8);
; #pragma unroll
;         for (int j = 0; j < 3; ++j) { const float wgt = (t - 2 + j) >= 0 ? 1.f : 0.f; unpack8(la[j], a); unpack8(lb[j], b);
;             const f32x4 w0 = *(const f32x4*)(conv_w_l + j * 1024 + c8) * wgt, w1 = *(const f32x4*)(conv_w_l + j * 1024 + c8 + 4) * wgt;
;             acc[0] += w0.x * (a[0] * b[0]); acc[1] += w0.y * (a[1] * b[1]); acc[2] += w0.z * (a[2] * b[2]); acc[3] += w0.w * (a[3] * b[3]);
;             acc[4] += w1.x * (a[4] * b[4]); acc[5] += w1.y * (a[5] * b[5]); acc[6] += w1.z * (a[6] * b[6]); acc[7] += w1.w * (a[7] * b[7]); }
;         unpack8(lg, a);
;         v4u o; o.x = pk2(a[0] * acc[0], a[1] * acc[1]); o.y = pk2(a[2] * acc[2], a[3] * acc[3]); o.z = pk2(a[4] * acc[4], a[5] * acc[5]); o.w = pk2(a[6] * acc[6], a[7] * acc[7]);
;         *(v4u*)(F.Y + (size_t)M * 1024 + (size_t)row * 1024 + c8) = o;
;     }
.Lpc_conv:
	s_mul_i32 s10, s10, 0x3000
	s_add_u32 s12, s86, s10
	s_addc_u32 s13, s87, 0
	v_and_b32_e32 v3, 0x7f, v1
	v_lshrrev_b32_e32 v2, 7, v1
	v_lshlrev_b32_e32 v8, 5, v3
	global_load_dwordx4 v[148:151], v8, s[12:13] offset:0
	global_load_dwordx4 v[152:155], v8, s[12:13] offset:16
	v_add_u32_e32 v8, 0x1000, v8
	global_load_dwordx4 v[156:159], v8, s[12:13] offset:0
	global_load_dwordx4 v[160:163], v8, s[12:13] offset:16
	v_add_u32_e32 v8, 0x1000, v8
	global_load_dwordx4 v[164:167], v8, s[12:13] offset:0
	global_load_dwordx4 v[168:171], v8, s[12:13] offset:16
	v_lshlrev_b32_e32 v8, 4, v3
	v_add_u32_e32 v19, 0x800, v8
	s_add_u32 s14, s14, 0x1000000
	s_addc_u32 s15, s15, 0
	v_lshlrev_b32_e32 v4, 2, v2
	v_and_b32_e32 v5, 0x7ff, v4
	v_mul_u32_u24_e32 v6, 0x3600, v5
	v_mul_u32_u24_e32 v7, 0x3600, v4
	v_add_u32_e32 v7, v7, v19
	v_lshl_add_u32 v16, v4, 11, v8
	v_min_u32_e32 v11, 0x6c00, v6
	v_sub_u32_e32 v12, v7, v11
	global_load_dwordx4 v[20:23], v12, s[96:97] offset:2048
	global_load_dwordx4 v[44:47], v12, s[96:97]
	v_min_u32_e32 v11, 0x3600, v6
	v_sub_u32_e32 v12, v7, v11
	global_load_dwordx4 v[24:27], v12, s[96:97] offset:2048
	global_load_dwordx4 v[48:51], v12, s[96:97]
	v_mov_b32_e32 v12, v7
	global_load_dwordx4 v[28:31], v12, s[96:97] offset:2048
	global_load_dwordx4 v[52:55], v12, s[96:97]
	v_add_u32_e32 v13, 0x1000, v12
	global_load_dwordx4 v[68:71], v13, s[96:97]
	v_add_u32_e32 v12, 0x3600, v7
	global_load_dwordx4 v[32:35], v12, s[96:97] offset:2048
	global_load_dwordx4 v[56:59], v12, s[96:97]
	v_add_u32_e32 v13, 0x1000, v12
	global_load_dwordx4 v[72:75], v13, s[96:97]
	v_add_u32_e32 v12, 0x6c00, v7
	global_load_dwordx4 v[36:39], v12, s[96:97] offset:2048
	global_load_dwordx4 v[60:63], v12, s[96:97]
	v_add_u32_e32 v13, 0x1000, v12
	global_load_dwordx4 v[76:79], v13, s[96:97]
	v_add_u32_e32 v12, 0xa200, v7
	global_load_dwordx4 v[40:43], v12, s[96:97] offset:2048
	global_load_dwordx4 v[64:67], v12, s[96:97]
	v_add_u32_e32 v13, 0x1000, v12
	global_load_dwordx4 v[80:83], v13, s[96:97]
	v_lshlrev_b32_e32 v4, 2, v2
	v_add_u32_e32 v4, 0x1000, v4
	v_and_b32_e32 v18, 0x7ff, v4
	v_mul_u32_u24_e32 v6, 0x3600, v18
	v_mul_u32_u24_e32 v7, 0x3600, v4
	v_add_u32_e32 v7, v7, v19
	v_lshl_add_u32 v17, v4, 11, v8
	v_min_u32_e32 v11, 0x6c00, v6
	v_sub_u32_e32 v12, v7, v11
	global_load_dwordx4 v[84:87], v12, s[96:97] offset:2048
	global_load_dwordx4 v[108:111], v12, s[96:97]
	v_min_u32_e32 v11, 0x3600, v6
	v_sub_u32_e32 v12, v7, v11
	global_load_dwordx4 v[88:91], v12, s[96:97] offset:2048
	global_load_dwordx4 v[112:115], v12, s[96:97]
	v_mov_b32_e32 v12, v7
	global_load_dwordx4 v[92:95], v12, s[96:97] offset:2048
	global_load_dwordx4 v[116:119], v12, s[96:97]
	v_add_u32_e32 v13, 0x1000, v12
	global_load_dwordx4 v[132:135], v13, s[96:97]
	v_add_u32_e32 v12, 0x3600, v7
	global_load_dwordx4 v[96:99], v12, s[96:97] offset:2048
	global_load_dwordx4 v[120:123], v12, s[96:97]
	v_add_u32_e32 v13, 0x1000, v12
	global_load_dwordx4 v[136:139], v13, s[96:97]
	v_add_u32_e32 v12, 0x6c00, v7
	global_load_dwordx4 v[100:103], v12, s[96:97] offset:2048
	global_load_dwordx4 v[124:127], v12, s[96:97]
	v_add_u32_e32 v13, 0x1000, v12
	global_load_dwordx4 v[140:143], v13, s[96:97]
	v_add_u32_e32 v12, 0xa200, v7
	global_load_dwordx4 v[104:107], v12, s[96:97] offset:2048
	global_load_dwordx4 v[128:131], v12, s[96:97]
	v_add_u32_e32 v13, 0x1000, v12
	global_load_dwordx4 v[144:147], v13, s[96:97]
	s_waitcnt vmcnt(16)
	v_cmp_le_u32_e32 vcc, 2, v5
	s_nop 1
	v_cndmask_b32_e32 v20, 0, v20, vcc
	v_cndmask_b32_e32 v21, 0, v21, vcc
	v_cndmask_b32_e32 v22, 0, v22, vcc
	v_cndmask_b32_e32 v23, 0, v23, vcc
	v_cmp_le_u32_e32 vcc, 1, v5
	s_nop 1
	v_cndmask_b32_e32 v24, 0, v24, vcc
	v_cndmask_b32_e32 v25, 0, v25, vcc
	v_cndmask_b32_e32 v26, 0, v26, vcc
	v_cndmask_b32_e32 v27, 0, v27, vcc
	v_lshlrev_b32_e32 v172, 16, v20
	v_and_b32_e32 v173, 0xffff0000, v20
	v_lshlrev_b32_e32 v174, 16, v44
	v_and_b32_e32 v175, 0xffff0000, v44
	v_mul_f32_e32 v194, v172, v174
	v_mul_f32_e32 v195, v173, v175
	v_lshlrev_b32_e32 v172, 16, v21
	v_and_b32_e32 v173, 0xffff0000, v21
	v_lshlrev_b32_e32 v174, 16, v45
	v_and_b32_e32 v175, 0xffff0000, v45
	v_mul_f32_e32 v196, v172, v174
	v_mul_f32_e32 v197, v173, v175
	v_lshlrev_b32_e32 v172, 16, v22
	v_and_b32_e32 v173, 0xffff0000, v22
	v_lshlrev_b32_e32 v174, 16, v46
	v_and_b32_e32 v175, 0xffff0000, v46
	v_mul_f32_e32 v198, v172, v174
	v_mul_f32_e32 v199, v173, v175
	v_lshlrev_b32_e32 v172, 16, v23
	v_and_b32_e32 v173, 0xffff0000, v23
	v_lshlrev_b32_e32 v174, 16, v47
	v_and_b32_e32 v175, 0xffff0000, v47
	v_mul_f32_e32 v200, v172, v174
	v_mul_f32_e32 v201, v173, v175
	v_lshlrev_b32_e32 v172, 16, v24
	v_and_b32_e32 v173, 0xffff0000, v24
	v_lshlrev_b32_e32 v174, 16, v48
	v_and_b32_e32 v175, 0xffff0000, v48
	v_mul_f32_e32 v202, v172, v174
	v_mul_f32_e32 v203, v173, v175
	v_lshlrev_b32_e32 v172, 16, v25
	v_and_b32_e32 v173, 0xffff0000, v25
	v_lshlrev_b32_e32 v174, 16, v49
	v_and_b32_e32 v175, 0xffff0000, v49
	v_mul_f32_e32 v204, v172, v174
	v_mul_f32_e32 v205, v173, v175
	v_lshlrev_b32_e32 v172, 16, v26
	v_and_b32_e32 v173, 0xffff0000, v26
	v_lshlrev_b32_e32 v174, 16, v50
	v_and_b32_e32 v175, 0xffff0000, v50
	v_mul_f32_e32 v206, v172, v174
	v_mul_f32_e32 v207, v173, v175
	v_lshlrev_b32_e32 v172, 16, v27
	v_and_b32_e32 v173, 0xffff0000, v27
	v_lshlrev_b32_e32 v174, 16, v51
	v_and_b32_e32 v175, 0xffff0000, v51
	v_mul_f32_e32 v208, v172, v174
	v_mul_f32_e32 v209, v173, v175
	v_lshlrev_b32_e32 v172, 16, v28
	v_and_b32_e32 v173, 0xffff0000, v28
	v_lshlrev_b32_e32 v174, 16, v52
	v_and_b32_e32 v175, 0xffff0000, v52
	v_mul_f32_e32 v210, v172, v174
	v_mul_f32_e32 v211, v173, v175
; __device__ __forceinline__ unsigned pk2(float lo, float hi) { return pg8::cvt_pk_bf16(lo, hi); }
; __device__ __forceinline__ void unpack8(const v4u w, float (&f)[8]) { f[0] = bflo(w.x); f[1] = bfhi(w.x); f[2] = bflo(w.y); f[3] = bfhi(w.y); f[4] = bflo(w.z); f[5] = bfhi(w.z); f[6] = bflo(w.w); f[7] = bfhi(w.w); }
; __device__ __forceinline__ void poolconv_phase(Frame& F, const float* conv_w_l) {
;     ...
; #pragma unroll
;         for (int j = 0; j < 3; ++j) { const float wgt = (t - 2 + j) >= 0 ? 1.f : 0.f; unpack8(la[j], a); unpack8(lb[j], b);
;             const f32x4 w0 = *(const f32x4*)(conv_w_l + j * 1024 + c8) * wgt, w1 = *(const f32x4*)(conv_w_l + j * 1024 + c8 + 4) * wgt;
;             acc[0] += w0.x * (a[0] * b[0]); acc[1] += w0.y * (a[1] * b[1]); acc[2] += w0.z * (a[2] * b[2]); acc[3] += w0.w * (a[3] * b[3]);
;             acc[4] += w1.x * (a[4] * b[4]); acc[5] += w1.y * (a[5] * b[5]); acc[6] += w1.z * (a[6] * b[6]); acc[7] += w1.w * (a[7] * b[7]); }
;         unpack8(lg, a);
;         v4u o; o.x = pk2(a[0] * acc[0], a[1] * acc[1]); o.y = pk2(a[2] * acc[2], a[3] * acc[3]); o.z = pk2(a[4] * acc[4], a[5] * acc[5]); o.w = pk2(a[6] * acc[6], a[7] * acc[7]);
;         *(v4u*)(F.Y + (size_t)M * 1024 + (size_t)row * 1024 + c8) = o;
	v_lshlrev_b32_e32 v172, 16, v29
	v_and_b32_e32 v173, 0xffff0000, v29
	v_lshlrev_b32_e32 v174, 16, v53
	v_and_b32_e32 v175, 0xffff0000, v53
	v_mul_f32_e32 v212, v172, v174
	v_mul_f32_e32 v213, v173, v175
	v_lshlrev_b32_e32 v172, 16, v30
	v_and_b32_e32 v173, 0xffff0000, v30
	v_lshlrev_b32_e32 v174, 16, v54
	v_and_b32_e32 v175, 0xffff0000, v54
	v_mul_f32_e32 v214, v172, v174
	v_mul_f32_e32 v215, v173, v175
	v_lshlrev_b32_e32 v172, 16, v31
	v_and_b32_e32 v173, 0xffff0000, v31
	v_lshlrev_b32_e32 v174, 16, v55
	v_and_b32_e32 v175, 0xffff0000, v55
	v_mul_f32_e32 v216, v172, v174
	v_mul_f32_e32 v217, v173, v175
	v_lshlrev_b32_e32 v172, 16, v32
	v_and_b32_e32 v173, 0xffff0000, v32
	v_lshlrev_b32_e32 v174, 16, v56
	v_and_b32_e32 v175, 0xffff0000, v56
	v_mul_f32_e32 v218, v172, v174
	v_mul_f32_e32 v219, v173, v175
	v_lshlrev_b32_e32 v172, 16, v33
	v_and_b32_e32 v173, 0xffff0000, v33
	v_lshlrev_b32_e32 v174, 16, v57
	v_and_b32_e32 v175, 0xffff0000, v57
	v_mul_f32_e32 v220, v172, v174
	v_mul_f32_e32 v221, v173, v175
	v_lshlrev_b32_e32 v172, 16, v34
	v_and_b32_e32 v173, 0xffff0000, v34
	v_lshlrev_b32_e32 v174, 16, v58
	v_and_b32_e32 v175, 0xffff0000, v58
	v_mul_f32_e32 v222, v172, v174
	v_mul_f32_e32 v223, v173, v175
	v_lshlrev_b32_e32 v172, 16, v35
	v_and_b32_e32 v173, 0xffff0000, v35
	v_lshlrev_b32_e32 v174, 16, v59
	v_and_b32_e32 v175, 0xffff0000, v59
	v_mul_f32_e32 v224, v172, v174
	v_mul_f32_e32 v225, v173, v175
	v_lshlrev_b32_e32 v172, 16, v36
	v_and_b32_e32 v173, 0xffff0000, v36
	v_lshlrev_b32_e32 v174, 16, v60
	v_and_b32_e32 v175, 0xffff0000, v60
	v_mul_f32_e32 v226, v172, v174
	v_mul_f32_e32 v227, v173, v175
	v_lshlrev_b32_e32 v172, 16, v37
	v_and_b32_e32 v173, 0xffff0000, v37
	v_lshlrev_b32_e32 v174, 16, v61
	v_and_b32_e32 v175, 0xffff0000, v61
	v_mul_f32_e32 v228, v172, v174
	v_mul_f32_e32 v229, v173, v175
	v_lshlrev_b32_e32 v172, 16, v38
	v_and_b32_e32 v173, 0xffff0000, v38
	v_lshlrev_b32_e32 v174, 16, v62
	v_and_b32_e32 v175, 0xffff0000, v62
	v_mul_f32_e32 v230, v172, v174
	v_mul_f32_e32 v231, v173, v175
	v_lshlrev_b32_e32 v172, 16, v39
	v_and_b32_e32 v173, 0xffff0000, v39
	v_lshlrev_b32_e32 v174, 16, v63
	v_and_b32_e32 v175, 0xffff0000, v63
	v_mul_f32_e32 v232, v172, v174
	v_mul_f32_e32 v233, v173, v175
	v_lshlrev_b32_e32 v172, 16, v40
	v_and_b32_e32 v173, 0xffff0000, v40
	v_lshlrev_b32_e32 v174, 16, v64
	v_and_b32_e32 v175, 0xffff0000, v64
	v_mul_f32_e32 v234, v172, v174
	v_mul_f32_e32 v235, v173, v175
	v_lshlrev_b32_e32 v172, 16, v41
	v_and_b32_e32 v173, 0xffff0000, v41
	v_lshlrev_b32_e32 v174, 16, v65
	v_and_b32_e32 v175, 0xffff0000, v65
	v_mul_f32_e32 v236, v172, v174
	v_mul_f32_e32 v237, v173, v175
	v_lshlrev_b32_e32 v172, 16, v42
	v_and_b32_e32 v173, 0xffff0000, v42
	v_lshlrev_b32_e32 v174, 16, v66
	v_and_b32_e32 v175, 0xffff0000, v66
	v_mul_f32_e32 v238, v172, v174
	v_mul_f32_e32 v239, v173, v175
	v_lshlrev_b32_e32 v172, 16, v43
	v_and_b32_e32 v173, 0xffff0000, v43
	v_lshlrev_b32_e32 v174, 16, v67
	v_and_b32_e32 v175, 0xffff0000, v67
	v_mul_f32_e32 v240, v172, v174
	v_mul_f32_e32 v241, v173, v175
	v_lshlrev_b32_e32 v172, 16, v68
	v_and_b32_e32 v173, 0xffff0000, v68
	v_mul_f32_e32 v176, v148, v194
	v_fmac_f32_e32 v176, v156, v202
	v_fmac_f32_e32 v176, v164, v210
	v_mul_f32_e32 v176, v172, v176
	v_mul_f32_e32 v177, v149, v195
	v_fmac_f32_e32 v177, v157, v203
	v_fmac_f32_e32 v177, v165, v211
	v_mul_f32_e32 v177, v173, v177
	v_lshlrev_b32_e32 v172, 16, v69
	v_and_b32_e32 v173, 0xffff0000, v69
	v_mul_f32_e32 v178, v150, v196
	v_fmac_f32_e32 v178, v158, v204
	v_fmac_f32_e32 v178, v166, v212
	v_mul_f32_e32 v178, v172, v178
	v_mul_f32_e32 v179, v151, v197
	v_fmac_f32_e32 v179, v159, v205
	v_fmac_f32_e32 v179, v167, v213
	v_mul_f32_e32 v179, v173, v179
	v_lshlrev_b32_e32 v172, 16, v70
	v_and_b32_e32 v173, 0xffff0000, v70
	v_mul_f32_e32 v180, v152, v198
	v_fmac_f32_e32 v180, v160, v206
	v_fmac_f32_e32 v180, v168, v214
	v_mul_f32_e32 v180, v172, v180
	v_mul_f32_e32 v181, v153, v199
	v_fmac_f32_e32 v181, v161, v207
	v_fmac_f32_e32 v181, v169, v215
	v_mul_f32_e32 v181, v173, v181
	v_lshlrev_b32_e32 v172, 16, v71
	v_and_b32_e32 v173, 0xffff0000, v71
	v_mul_f32_e32 v182, v154, v200
	v_fmac_f32_e32 v182, v162, v208
	v_fmac_f32_e32 v182, v170, v216
	v_mul_f32_e32 v182, v172, v182
	v_mul_f32_e32 v183, v155, v201
	v_fmac_f32_e32 v183, v163, v209
	v_fmac_f32_e32 v183, v171, v217
	v_mul_f32_e32 v183, v173, v183
	v_cvt_pk_bf16_f32 v184, v176, v177
	v_cvt_pk_bf16_f32 v185, v178, v179
	v_cvt_pk_bf16_f32 v186, v180, v181
	v_cvt_pk_bf16_f32 v187, v182, v183
	global_store_dwordx4 v16, v[184:187], s[14:15]
	s_nop 1
	v_lshlrev_b32_e32 v172, 16, v72
	v_and_b32_e32 v173, 0xffff0000, v72
	v_mul_f32_e32 v176, v148, v202
	v_fmac_f32_e32 v176, v156, v210
	v_fmac_f32_e32 v176, v164, v218
	v_mul_f32_e32 v176, v172, v176
	v_mul_f32_e32 v177, v149, v203
	v_fmac_f32_e32 v177, v157, v211
	v_fmac_f32_e32 v177, v165, v219
	v_mul_f32_e32 v177, v173, v177
	v_lshlrev_b32_e32 v172, 16, v73
	v_and_b32_e32 v173, 0xffff0000, v73
	v_mul_f32_e32 v178, v150, v204
	v_fmac_f32_e32 v178, v158, v212
	v_fmac_f32_e32 v178, v166, v220
	v_mul_f32_e32 v178, v172, v178
	v_mul_f32_e32 v179, v151, v205
	v_fmac_f32_e32 v179, v159, v213
	v_fmac_f32_e32 v179, v167, v221
	v_mul_f32_e32 v179, v173, v179
	v_lshlrev_b32_e32 v172, 16, v74
	v_and_b32_e32 v173, 0xffff0000, v74
	v_mul_f32_e32 v180, v152, v206
	v_fmac_f32_e32 v180, v160, v214
	v_fmac_f32_e32 v180, v168, v222
	v_mul_f32_e32 v180, v172, v180
	v_mul_f32_e32 v181, v153, v207
	v_fmac_f32_e32 v181, v161, v215
	v_fmac_f32_e32 v181, v169, v223
	v_mul_f32_e32 v181, v173, v181
	v_lshlrev_b32_e32 v172, 16, v75
	v_and_b32_e32 v173, 0xffff0000, v75
; __device__ __forceinline__ unsigned pk2(float lo, float hi) { return pg8::cvt_pk_bf16(lo, hi); }
; __device__ __forceinline__ void unpack8(const v4u w, float (&f)[8]) { f[0] = bflo(w.x); f[1] = bfhi(w.x); f[2] = bflo(w.y); f[3] = bfhi(w.y); f[4] = bflo(w.z); f[5] = bfhi(w.z); f[6] = bflo(w.w); f[7] = bfhi(w.w); }
; __device__ __forceinline__ void poolconv_phase(Frame& F, const float* conv_w_l) {
;     ...
; #pragma unroll
;         for (int j = 0; j < 3; ++j) { const float wgt = (t - 2 + j) >= 0 ? 1.f : 0.f; unpack8(la[j], a); unpack8(lb[j], b);
;             const f32x4 w0 = *(const f32x4*)(conv_w_l + j * 1024 + c8) * wgt, w1 = *(const f32x4*)(conv_w_l + j * 1024 + c8 + 4) * wgt;
;             acc[0] += w0.x * (a[0] * b[0]); acc[1] += w0.y * (a[1] * b[1]); acc[2] += w0.z * (a[2] * b[2]); acc[3] += w0.w * (a[3] * b[3]);
;             acc[4] += w1.x * (a[4] * b[4]); acc[5] += w1.y * (a[5] * b[5]); acc[6] += w1.z * (a[6] * b[6]); acc[7] += w1.w * (a[7] * b[7]); }
;         unpack8(lg, a);
;         v4u o; o.x = pk2(a[0] * acc[0], a[1] * acc[1]); o.y = pk2(a[2] * acc[2], a[3] * acc[3]); o.z = pk2(a[4] * acc[4], a[5] * acc[5]); o.w = pk2(a[6] * acc[6], a[7] * acc[7]);
;         *(v4u*)(F.Y + (size_t)M * 1024 + (size_t)row * 1024 + c8) = o;
	v_mul_f32_e32 v182, v154, v208
	v_fmac_f32_e32 v182, v162, v216
	v_fmac_f32_e32 v182, v170, v224
	v_mul_f32_e32 v182, v172, v182
	v_mul_f32_e32 v183, v155, v209
	v_fmac_f32_e32 v183, v163, v217
	v_fmac_f32_e32 v183, v171, v225
	v_mul_f32_e32 v183, v173, v183
	v_cvt_pk_bf16_f32 v184, v176, v177
	v_cvt_pk_bf16_f32 v185, v178, v179
	v_cvt_pk_bf16_f32 v186, v180, v181
	v_cvt_pk_bf16_f32 v187, v182, v183
	v_add_u32_e32 v13, 0x800, v16
	global_store_dwordx4 v13, v[184:187], s[14:15]
	s_nop 1
	v_lshlrev_b32_e32 v172, 16, v76
	v_and_b32_e32 v173, 0xffff0000, v76
	v_mul_f32_e32 v176, v148, v210
	v_fmac_f32_e32 v176, v156, v218
	v_fmac_f32_e32 v176, v164, v226
	v_mul_f32_e32 v176, v172, v176
	v_mul_f32_e32 v177, v149, v211
	v_fmac_f32_e32 v177, v157, v219
	v_fmac_f32_e32 v177, v165, v227
	v_mul_f32_e32 v177, v173, v177
	v_lshlrev_b32_e32 v172, 16, v77
	v_and_b32_e32 v173, 0xffff0000, v77
	v_mul_f32_e32 v178, v150, v212
	v_fmac_f32_e32 v178, v158, v220
	v_fmac_f32_e32 v178, v166, v228
	v_mul_f32_e32 v178, v172, v178
	v_mul_f32_e32 v179, v151, v213
	v_fmac_f32_e32 v179, v159, v221
	v_fmac_f32_e32 v179, v167, v229
	v_mul_f32_e32 v179, v173, v179
	v_lshlrev_b32_e32 v172, 16, v78
	v_and_b32_e32 v173, 0xffff0000, v78
	v_mul_f32_e32 v180, v152, v214
	v_fmac_f32_e32 v180, v160, v222
	v_fmac_f32_e32 v180, v168, v230
	v_mul_f32_e32 v180, v172, v180
	v_mul_f32_e32 v181, v153, v215
	v_fmac_f32_e32 v181, v161, v223
	v_fmac_f32_e32 v181, v169, v231
	v_mul_f32_e32 v181, v173, v181
	v_lshlrev_b32_e32 v172, 16, v79
	v_and_b32_e32 v173, 0xffff0000, v79
	v_mul_f32_e32 v182, v154, v216
	v_fmac_f32_e32 v182, v162, v224
	v_fmac_f32_e32 v182, v170, v232
	v_mul_f32_e32 v182, v172, v182
	v_mul_f32_e32 v183, v155, v217
	v_fmac_f32_e32 v183, v163, v225
	v_fmac_f32_e32 v183, v171, v233
	v_mul_f32_e32 v183, v173, v183
	v_cvt_pk_bf16_f32 v184, v176, v177
	v_cvt_pk_bf16_f32 v185, v178, v179
	v_cvt_pk_bf16_f32 v186, v180, v181
	v_cvt_pk_bf16_f32 v187, v182, v183
	v_add_u32_e32 v13, 0x1000, v16
	global_store_dwordx4 v13, v[184:187], s[14:15]
	s_nop 1
	v_lshlrev_b32_e32 v172, 16, v80
	v_and_b32_e32 v173, 0xffff0000, v80
	v_mul_f32_e32 v176, v148, v218
	v_fmac_f32_e32 v176, v156, v226
	v_fmac_f32_e32 v176, v164, v234
	v_mul_f32_e32 v176, v172, v176
	v_mul_f32_e32 v177, v149, v219
	v_fmac_f32_e32 v177, v157, v227
	v_fmac_f32_e32 v177, v165, v235
	v_mul_f32_e32 v177, v173, v177
	v_lshlrev_b32_e32 v172, 16, v81
	v_and_b32_e32 v173, 0xffff0000, v81
	v_mul_f32_e32 v178, v150, v220
	v_fmac_f32_e32 v178, v158, v228
	v_fmac_f32_e32 v178, v166, v236
	v_mul_f32_e32 v178, v172, v178
	v_mul_f32_e32 v179, v151, v221
	v_fmac_f32_e32 v179, v159, v229
	v_fmac_f32_e32 v179, v167, v237
	v_mul_f32_e32 v179, v173, v179
	v_lshlrev_b32_e32 v172, 16, v82
	v_and_b32_e32 v173, 0xffff0000, v82
	v_mul_f32_e32 v180, v152, v222
	v_fmac_f32_e32 v180, v160, v230
	v_fmac_f32_e32 v180, v168, v238
	v_mul_f32_e32 v180, v172, v180
	v_mul_f32_e32 v181, v153, v223
	v_fmac_f32_e32 v181, v161, v231
	v_fmac_f32_e32 v181, v169, v239
	v_mul_f32_e32 v181, v173, v181
	v_lshlrev_b32_e32 v172, 16, v83
	v_and_b32_e32 v173, 0xffff0000, v83
	v_mul_f32_e32 v182, v154, v224
	v_fmac_f32_e32 v182, v162, v232
	v_fmac_f32_e32 v182, v170, v240
	v_mul_f32_e32 v182, v172, v182
	v_mul_f32_e32 v183, v155, v225
	v_fmac_f32_e32 v183, v163, v233
	v_fmac_f32_e32 v183, v171, v241
	v_mul_f32_e32 v183, v173, v183
	v_cvt_pk_bf16_f32 v184, v176, v177
	v_cvt_pk_bf16_f32 v185, v178, v179
	v_cvt_pk_bf16_f32 v186, v180, v181
	v_cvt_pk_bf16_f32 v187, v182, v183
	v_add_u32_e32 v13, 0x1800, v16
	global_store_dwordx4 v13, v[184:187], s[14:15]
	s_nop 1
	s_waitcnt vmcnt(4)
	v_cmp_le_u32_e32 vcc, 2, v18
	s_nop 1
	v_cndmask_b32_e32 v84, 0, v84, vcc
	v_cndmask_b32_e32 v85, 0, v85, vcc
	v_cndmask_b32_e32 v86, 0, v86, vcc
	v_cndmask_b32_e32 v87, 0, v87, vcc
	v_cmp_le_u32_e32 vcc, 1, v18
	s_nop 1
	v_cndmask_b32_e32 v88, 0, v88, vcc
	v_cndmask_b32_e32 v89, 0, v89, vcc
	v_cndmask_b32_e32 v90, 0, v90, vcc
	v_cndmask_b32_e32 v91, 0, v91, vcc
	v_lshlrev_b32_e32 v172, 16, v84
	v_and_b32_e32 v173, 0xffff0000, v84
	v_lshlrev_b32_e32 v174, 16, v108
	v_and_b32_e32 v175, 0xffff0000, v108
	v_mul_f32_e32 v194, v172, v174
	v_mul_f32_e32 v195, v173, v175
	v_lshlrev_b32_e32 v172, 16, v85
	v_and_b32_e32 v173, 0xffff0000, v85
	v_lshlrev_b32_e32 v174, 16, v109
	v_and_b32_e32 v175, 0xffff0000, v109
	v_mul_f32_e32 v196, v172, v174
	v_mul_f32_e32 v197, v173, v175
	v_lshlrev_b32_e32 v172, 16, v86
	v_and_b32_e32 v173, 0xffff0000, v86
	v_lshlrev_b32_e32 v174, 16, v110
	v_and_b32_e32 v175, 0xffff0000, v110
	v_mul_f32_e32 v198, v172, v174
	v_mul_f32_e32 v199, v173, v175
	v_lshlrev_b32_e32 v172, 16, v87
	v_and_b32_e32 v173, 0xffff0000, v87
	v_lshlrev_b32_e32 v174, 16, v111
	v_and_b32_e32 v175, 0xffff0000, v111
	v_mul_f32_e32 v200, v172, v174
	v_mul_f32_e32 v201, v173, v175
	v_lshlrev_b32_e32 v172, 16, v88
	v_and_b32_e32 v173, 0xffff0000, v88
	v_lshlrev_b32_e32 v174, 16, v112
	v_and_b32_e32 v175, 0xffff0000, v112
	v_mul_f32_e32 v202, v172, v174
	v_mul_f32_e32 v203, v173, v175
	v_lshlrev_b32_e32 v172, 16, v89
	v_and_b32_e32 v173, 0xffff0000, v89
	v_lshlrev_b32_e32 v174, 16, v113
	v_and_b32_e32 v175, 0xffff0000, v113
	v_mul_f32_e32 v204, v172, v174
	v_mul_f32_e32 v205, v173, v175
	v_lshlrev_b32_e32 v172, 16, v90
	v_and_b32_e32 v173, 0xffff0000, v90
	v_lshlrev_b32_e32 v174, 16, v114
	v_and_b32_e32 v175, 0xffff0000, v114
	v_mul_f32_e32 v206, v172, v174
	v_mul_f32_e32 v207, v173, v175
	v_lshlrev_b32_e32 v172, 16, v91
	v_and_b32_e32 v173, 0xffff0000, v91
	v_lshlrev_b32_e32 v174, 16, v115
	v_and_b32_e32 v175, 0xffff0000, v115
	v_mul_f32_e32 v208, v172, v174
	v_mul_f32_e32 v209, v173, v175
; __device__ __forceinline__ unsigned pk2(float lo, float hi) { return pg8::cvt_pk_bf16(lo, hi); }
; __device__ __forceinline__ void unpack8(const v4u w, float (&f)[8]) { f[0] = bflo(w.x); f[1] = bfhi(w.x); f[2] = bflo(w.y); f[3] = bfhi(w.y); f[4] = bflo(w.z); f[5] = bfhi(w.z); f[6] = bflo(w.w); f[7] = bfhi(w.w); }
; __device__ __forceinline__ void poolconv_phase(Frame& F, const float* conv_w_l) {
;     ...
; #pragma unroll
;         for (int j = 0; j < 3; ++j) { const float wgt = (t - 2 + j) >= 0 ? 1.f : 0.f; unpack8(la[j], a); unpack8(lb[j], b);
;             const f32x4 w0 = *(const f32x4*)(conv_w_l + j * 1024 + c8) * wgt, w1 = *(const f32x4*)(conv_w_l + j * 1024 + c8 + 4) * wgt;
;             acc[0] += w0.x * (a[0] * b[0]); acc[1] += w0.y * (a[1] * b[1]); acc[2] += w0.z * (a[2] * b[2]); acc[3] += w0.w * (a[3] * b[3]);
;             acc[4] += w1.x * (a[4] * b[4]); acc[5] += w1.y * (a[5] * b[5]); acc[6] += w1.z * (a[6] * b[6]); acc[7] += w1.w * (a[7] * b[7]); }
;         unpack8(lg, a);
;         v4u o; o.x = pk2(a[0] * acc[0], a[1] * acc[1]); o.y = pk2(a[2] * acc[2], a[3] * acc[3]); o.z = pk2(a[4] * acc[4], a[5] * acc[5]); o.w = pk2(a[6] * acc[6], a[7] * acc[7]);
;         *(v4u*)(F.Y + (size_t)M * 1024 + (size_t)row * 1024 + c8) = o;
	v_lshlrev_b32_e32 v172, 16, v92
	v_and_b32_e32 v173, 0xffff0000, v92
	v_lshlrev_b32_e32 v174, 16, v116
	v_and_b32_e32 v175, 0xffff0000, v116
	v_mul_f32_e32 v210, v172, v174
	v_mul_f32_e32 v211, v173, v175
	v_lshlrev_b32_e32 v172, 16, v93
	v_and_b32_e32 v173, 0xffff0000, v93
	v_lshlrev_b32_e32 v174, 16, v117
	v_and_b32_e32 v175, 0xffff0000, v117
	v_mul_f32_e32 v212, v172, v174
	v_mul_f32_e32 v213, v173, v175
	v_lshlrev_b32_e32 v172, 16, v94
	v_and_b32_e32 v173, 0xffff0000, v94
	v_lshlrev_b32_e32 v174, 16, v118
	v_and_b32_e32 v175, 0xffff0000, v118
	v_mul_f32_e32 v214, v172, v174
	v_mul_f32_e32 v215, v173, v175
	v_lshlrev_b32_e32 v172, 16, v95
	v_and_b32_e32 v173, 0xffff0000, v95
	v_lshlrev_b32_e32 v174, 16, v119
	v_and_b32_e32 v175, 0xffff0000, v119
	v_mul_f32_e32 v216, v172, v174
	v_mul_f32_e32 v217, v173, v175
	v_lshlrev_b32_e32 v172, 16, v96
	v_and_b32_e32 v173, 0xffff0000, v96
	v_lshlrev_b32_e32 v174, 16, v120
	v_and_b32_e32 v175, 0xffff0000, v120
	v_mul_f32_e32 v218, v172, v174
	v_mul_f32_e32 v219, v173, v175
	v_lshlrev_b32_e32 v172, 16, v97
	v_and_b32_e32 v173, 0xffff0000, v97
	v_lshlrev_b32_e32 v174, 16, v121
	v_and_b32_e32 v175, 0xffff0000, v121
	v_mul_f32_e32 v220, v172, v174
	v_mul_f32_e32 v221, v173, v175
	v_lshlrev_b32_e32 v172, 16, v98
	v_and_b32_e32 v173, 0xffff0000, v98
	v_lshlrev_b32_e32 v174, 16, v122
	v_and_b32_e32 v175, 0xffff0000, v122
	v_mul_f32_e32 v222, v172, v174
	v_mul_f32_e32 v223, v173, v175
	v_lshlrev_b32_e32 v172, 16, v99
	v_and_b32_e32 v173, 0xffff0000, v99
	v_lshlrev_b32_e32 v174, 16, v123
	v_and_b32_e32 v175, 0xffff0000, v123
	v_mul_f32_e32 v224, v172, v174
	v_mul_f32_e32 v225, v173, v175
	v_lshlrev_b32_e32 v172, 16, v100
	v_and_b32_e32 v173, 0xffff0000, v100
	v_lshlrev_b32_e32 v174, 16, v124
	v_and_b32_e32 v175, 0xffff0000, v124
	v_mul_f32_e32 v226, v172, v174
	v_mul_f32_e32 v227, v173, v175
	v_lshlrev_b32_e32 v172, 16, v101
	v_and_b32_e32 v173, 0xffff0000, v101
	v_lshlrev_b32_e32 v174, 16, v125
	v_and_b32_e32 v175, 0xffff0000, v125
	v_mul_f32_e32 v228, v172, v174
	v_mul_f32_e32 v229, v173, v175
	v_lshlrev_b32_e32 v172, 16, v102
	v_and_b32_e32 v173, 0xffff0000, v102
	v_lshlrev_b32_e32 v174, 16, v126
	v_and_b32_e32 v175, 0xffff0000, v126
	v_mul_f32_e32 v230, v172, v174
	v_mul_f32_e32 v231, v173, v175
	v_lshlrev_b32_e32 v172, 16, v103
	v_and_b32_e32 v173, 0xffff0000, v103
	v_lshlrev_b32_e32 v174, 16, v127
	v_and_b32_e32 v175, 0xffff0000, v127
	v_mul_f32_e32 v232, v172, v174
	v_mul_f32_e32 v233, v173, v175
	v_lshlrev_b32_e32 v172, 16, v104
	v_and_b32_e32 v173, 0xffff0000, v104
	v_lshlrev_b32_e32 v174, 16, v128
	v_and_b32_e32 v175, 0xffff0000, v128
	v_mul_f32_e32 v234, v172, v174
	v_mul_f32_e32 v235, v173, v175
	v_lshlrev_b32_e32 v172, 16, v105
	v_and_b32_e32 v173, 0xffff0000, v105
	v_lshlrev_b32_e32 v174, 16, v129
	v_and_b32_e32 v175, 0xffff0000, v129
	v_mul_f32_e32 v236, v172, v174
	v_mul_f32_e32 v237, v173, v175
	v_lshlrev_b32_e32 v172, 16, v106
	v_and_b32_e32 v173, 0xffff0000, v106
	v_lshlrev_b32_e32 v174, 16, v130
	v_and_b32_e32 v175, 0xffff0000, v130
	v_mul_f32_e32 v238, v172, v174
	v_mul_f32_e32 v239, v173, v175
	v_lshlrev_b32_e32 v172, 16, v107
	v_and_b32_e32 v173, 0xffff0000, v107
	v_lshlrev_b32_e32 v174, 16, v131
	v_and_b32_e32 v175, 0xffff0000, v131
	v_mul_f32_e32 v240, v172, v174
	v_mul_f32_e32 v241, v173, v175
	v_lshlrev_b32_e32 v172, 16, v132
	v_and_b32_e32 v173, 0xffff0000, v132
	v_mul_f32_e32 v176, v148, v194
	v_fmac_f32_e32 v176, v156, v202
	v_fmac_f32_e32 v176, v164, v210
	v_mul_f32_e32 v176, v172, v176
	v_mul_f32_e32 v177, v149, v195
	v_fmac_f32_e32 v177, v157, v203
	v_fmac_f32_e32 v177, v165, v211
	v_mul_f32_e32 v177, v173, v177
	v_lshlrev_b32_e32 v172, 16, v133
	v_and_b32_e32 v173, 0xffff0000, v133
	v_mul_f32_e32 v178, v150, v196
	v_fmac_f32_e32 v178, v158, v204
	v_fmac_f32_e32 v178, v166, v212
	v_mul_f32_e32 v178, v172, v178
	v_mul_f32_e32 v179, v151, v197
	v_fmac_f32_e32 v179, v159, v205
	v_fmac_f32_e32 v179, v167, v213
	v_mul_f32_e32 v179, v173, v179
	v_lshlrev_b32_e32 v172, 16, v134
	v_and_b32_e32 v173, 0xffff0000, v134
	v_mul_f32_e32 v180, v152, v198
	v_fmac_f32_e32 v180, v160, v206
	v_fmac_f32_e32 v180, v168, v214
	v_mul_f32_e32 v180, v172, v180
	v_mul_f32_e32 v181, v153, v199
	v_fmac_f32_e32 v181, v161, v207
	v_fmac_f32_e32 v181, v169, v215
	v_mul_f32_e32 v181, v173, v181
	v_lshlrev_b32_e32 v172, 16, v135
	v_and_b32_e32 v173, 0xffff0000, v135
	v_mul_f32_e32 v182, v154, v200
	v_fmac_f32_e32 v182, v162, v208
	v_fmac_f32_e32 v182, v170, v216
	v_mul_f32_e32 v182, v172, v182
	v_mul_f32_e32 v183, v155, v201
	v_fmac_f32_e32 v183, v163, v209
	v_fmac_f32_e32 v183, v171, v217
	v_mul_f32_e32 v183, v173, v183
	v_cvt_pk_bf16_f32 v184, v176, v177
	v_cvt_pk_bf16_f32 v185, v178, v179
	v_cvt_pk_bf16_f32 v186, v180, v181
	v_cvt_pk_bf16_f32 v187, v182, v183
; __device__ __forceinline__ unsigned pk2(float lo, float hi) { return pg8::cvt_pk_bf16(lo, hi); }
; __device__ __forceinline__ void unpack8(const v4u w, float (&f)[8]) { f[0] = bflo(w.x); f[1] = bfhi(w.x); f[2] = bflo(w.y); f[3] = bfhi(w.y); f[4] = bflo(w.z); f[5] = bfhi(w.z); f[6] = bflo(w.w); f[7] = bfhi(w.w); }
; __device__ __forceinline__ void poolconv_phase(Frame& F, const float* conv_w_l) {
;     ...
; #pragma unroll
;         for (int j = 0; j < 3; ++j) { const float wgt = (t - 2 + j) >= 0 ? 1.f : 0.f; unpack8(la[j], a); unpack8(lb[j], b);
;             const f32x4 w0 = *(const f32x4*)(conv_w_l + j * 1024 + c8) * wgt, w1 = *(const f32x4*)(conv_w_l + j * 1024 + c8 + 4) * wgt;
;             acc[0] += w0.x * (a[0] * b[0]); acc[1] += w0.y * (a[1] * b[1]); acc[2] += w0.z * (a[2] * b[2]); acc[3] += w0.w * (a[3] * b[3]);
;             acc[4] += w1.x * (a[4] * b[4]); acc[5] += w1.y * (a[5] * b[5]); acc[6] += w1.z * (a[6] * b[6]); acc[7] += w1.w * (a[7] * b[7]); }
;         unpack8(lg, a);
;         v4u o; o.x = pk2(a[0] * acc[0], a[1] * acc[1]); o.y = pk2(a[2] * acc[2], a[3] * acc[3]); o.z = pk2(a[4] * acc[4], a[5] * acc[5]); o.w = pk2(a[6] * acc[6], a[7] * acc[7]);
;         *(v4u*)(F.Y + (size_t)M * 1024 + (size_t)row * 1024 + c8) = o;
	global_store_dwordx4 v17, v[184:187], s[14:15]
	s_nop 1
	v_lshlrev_b32_e32 v172, 16, v136
	v_and_b32_e32 v173, 0xffff0000, v136
	v_mul_f32_e32 v176, v148, v202
	v_fmac_f32_e32 v176, v156, v210
	v_fmac_f32_e32 v176, v164, v218
	v_mul_f32_e32 v176, v172, v176
	v_mul_f32_e32 v177, v149, v203
	v_fmac_f32_e32 v177, v157, v211
	v_fmac_f32_e32 v177, v165, v219
	v_mul_f32_e32 v177, v173, v177
	v_lshlrev_b32_e32 v172, 16, v137
	v_and_b32_e32 v173, 0xffff0000, v137
	v_mul_f32_e32 v178, v150, v204
	v_fmac_f32_e32 v178, v158, v212
	v_fmac_f32_e32 v178, v166, v220
	v_mul_f32_e32 v178, v172, v178
	v_mul_f32_e32 v179, v151, v205
	v_fmac_f32_e32 v179, v159, v213
	v_fmac_f32_e32 v179, v167, v221
	v_mul_f32_e32 v179, v173, v179
	v_lshlrev_b32_e32 v172, 16, v138
	v_and_b32_e32 v173, 0xffff0000, v138
	v_mul_f32_e32 v180, v152, v206
	v_fmac_f32_e32 v180, v160, v214
	v_fmac_f32_e32 v180, v168, v222
	v_mul_f32_e32 v180, v172, v180
	v_mul_f32_e32 v181, v153, v207
	v_fmac_f32_e32 v181, v161, v215
	v_fmac_f32_e32 v181, v169, v223
	v_mul_f32_e32 v181, v173, v181
	v_lshlrev_b32_e32 v172, 16, v139
	v_and_b32_e32 v173, 0xffff0000, v139
	v_mul_f32_e32 v182, v154, v208
	v_fmac_f32_e32 v182, v162, v216
	v_fmac_f32_e32 v182, v170, v224
	v_mul_f32_e32 v182, v172, v182
	v_mul_f32_e32 v183, v155, v209
	v_fmac_f32_e32 v183, v163, v217
	v_fmac_f32_e32 v183, v171, v225
	v_mul_f32_e32 v183, v173, v183
	v_cvt_pk_bf16_f32 v184, v176, v177
	v_cvt_pk_bf16_f32 v185, v178, v179
	v_cvt_pk_bf16_f32 v186, v180, v181
	v_cvt_pk_bf16_f32 v187, v182, v183
	v_add_u32_e32 v13, 0x800, v17
	global_store_dwordx4 v13, v[184:187], s[14:15]
	s_nop 1
	v_lshlrev_b32_e32 v172, 16, v140
	v_and_b32_e32 v173, 0xffff0000, v140
	v_mul_f32_e32 v176, v148, v210
	v_fmac_f32_e32 v176, v156, v218
	v_fmac_f32_e32 v176, v164, v226
	v_mul_f32_e32 v176, v172, v176
	v_mul_f32_e32 v177, v149, v211
	v_fmac_f32_e32 v177, v157, v219
	v_fmac_f32_e32 v177, v165, v227
	v_mul_f32_e32 v177, v173, v177
	v_lshlrev_b32_e32 v172, 16, v141
	v_and_b32_e32 v173, 0xffff0000, v141
	v_mul_f32_e32 v178, v150, v212
	v_fmac_f32_e32 v178, v158, v220
	v_fmac_f32_e32 v178, v166, v228
	v_mul_f32_e32 v178, v172, v178
	v_mul_f32_e32 v179, v151, v213
	v_fmac_f32_e32 v179, v159, v221
	v_fmac_f32_e32 v179, v167, v229
	v_mul_f32_e32 v179, v173, v179
	v_lshlrev_b32_e32 v172, 16, v142
	v_and_b32_e32 v173, 0xffff0000, v142
	v_mul_f32_e32 v180, v152, v214
	v_fmac_f32_e32 v180, v160, v222
	v_fmac_f32_e32 v180, v168, v230
	v_mul_f32_e32 v180, v172, v180
	v_mul_f32_e32 v181, v153, v215
	v_fmac_f32_e32 v181, v161, v223
	v_fmac_f32_e32 v181, v169, v231
	v_mul_f32_e32 v181, v173, v181
	v_lshlrev_b32_e32 v172, 16, v143
	v_and_b32_e32 v173, 0xffff0000, v143
	v_mul_f32_e32 v182, v154, v216
	v_fmac_f32_e32 v182, v162, v224
	v_fmac_f32_e32 v182, v170, v232
	v_mul_f32_e32 v182, v172, v182
	v_mul_f32_e32 v183, v155, v217
	v_fmac_f32_e32 v183, v163, v225
	v_fmac_f32_e32 v183, v171, v233
	v_mul_f32_e32 v183, v173, v183
	v_cvt_pk_bf16_f32 v184, v176, v177
	v_cvt_pk_bf16_f32 v185, v178, v179
	v_cvt_pk_bf16_f32 v186, v180, v181
	v_cvt_pk_bf16_f32 v187, v182, v183
	v_add_u32_e32 v13, 0x1000, v17
	global_store_dwordx4 v13, v[184:187], s[14:15]
	s_nop 1
	v_lshlrev_b32_e32 v172, 16, v144
	v_and_b32_e32 v173, 0xffff0000, v144
	v_mul_f32_e32 v176, v148, v218
	v_fmac_f32_e32 v176, v156, v226
	v_fmac_f32_e32 v176, v164, v234
	v_mul_f32_e32 v176, v172, v176
	v_mul_f32_e32 v177, v149, v219
	v_fmac_f32_e32 v177, v157, v227
	v_fmac_f32_e32 v177, v165, v235
	v_mul_f32_e32 v177, v173, v177
	v_lshlrev_b32_e32 v172, 16, v145
	v_and_b32_e32 v173, 0xffff0000, v145
	v_mul_f32_e32 v178, v150, v220
	v_fmac_f32_e32 v178, v158, v228
	v_fmac_f32_e32 v178, v166, v236
	v_mul_f32_e32 v178, v172, v178
	v_mul_f32_e32 v179, v151, v221
	v_fmac_f32_e32 v179, v159, v229
	v_fmac_f32_e32 v179, v167, v237
	v_mul_f32_e32 v179, v173, v179
	v_lshlrev_b32_e32 v172, 16, v146
	v_and_b32_e32 v173, 0xffff0000, v146
	v_mul_f32_e32 v180, v152, v222
	v_fmac_f32_e32 v180, v160, v230
	v_fmac_f32_e32 v180, v168, v238
	v_mul_f32_e32 v180, v172, v180
	v_mul_f32_e32 v181, v153, v223
	v_fmac_f32_e32 v181, v161, v231
	v_fmac_f32_e32 v181, v169, v239
	v_mul_f32_e32 v181, v173, v181
	v_lshlrev_b32_e32 v172, 16, v147
	v_and_b32_e32 v173, 0xffff0000, v147
	v_mul_f32_e32 v182, v154, v224
	v_fmac_f32_e32 v182, v162, v232
	v_fmac_f32_e32 v182, v170, v240
	v_mul_f32_e32 v182, v172, v182
	v_mul_f32_e32 v183, v155, v225
	v_fmac_f32_e32 v183, v163, v233
	v_fmac_f32_e32 v183, v171, v241
	v_mul_f32_e32 v183, v173, v183
	v_cvt_pk_bf16_f32 v184, v176, v177
	v_cvt_pk_bf16_f32 v185, v178, v179
	v_cvt_pk_bf16_f32 v186, v180, v181
	v_cvt_pk_bf16_f32 v187, v182, v183
	v_add_u32_e32 v13, 0x1800, v17
	global_store_dwordx4 v13, v[184:187], s[14:15]
	s_nop 1
	s_movk_i32 s8, 0x1000
	s_mov_b32 s20, 0xff800000
	s_mov_b64 s[2:3], exec
